# speedup vs baseline: 1.0164x; 1.0164x over previous
_Z12k1_colsum_q8PKfPjPfS2_:
	s_load_dwordx8 s[4:11], s[0:1], 0x0
	v_and_b32_e32 v1, 63, v0
	v_lshrrev_b32_e32 v41, 6, v0
	s_lshl_b32 s12, s2, 3
	s_nop 0
	v_readfirstlane_b32 s14, v41
	s_add_u32 s12, s12, s14
	s_cmp_lt_u32 s12, 0x6a0
	s_cselect_b32 s29, 1, 0
	v_lshlrev_b32_e32 v34, 4, v1
	v_min_u32_e32 v35, 57, v1
	v_lshlrev_b32_e32 v35, 4, v35
	v_cmp_gt_u32_e64 s[18:19], 58, v1
	s_lshl_b32 s35, s14, 13
	s_add_u32 s36, s35, 0x1000
	v_add_u32_e32 v38, s35, v34
	v_lshrrev_b32_e32 v41, 5, v1
	v_mov_b32_e32 v42, 0xc35000
	v_mul_lo_u32 v39, v41, v42
	v_and_b32_e32 v42, 31, v1
	v_lshl_add_u32 v39, v42, 2, v39
	v_mov_b32_e32 v2, 0
	v_mov_b32_e32 v3, 0
	v_mov_b32_e32 v4, 0
	v_mov_b32_e32 v5, 0
	v_mov_b32_e32 v6, 0
	v_mov_b32_e32 v7, 0
	v_mov_b32_e32 v8, 0
	v_mov_b32_e32 v9, 0
	v_mov_b32_e32 v10, 0
	v_mov_b32_e32 v11, 0
	v_mov_b32_e32 v12, 0
	v_mov_b32_e32 v13, 0
	v_mov_b32_e32 v14, 0
	v_mov_b32_e32 v15, 0
	v_mov_b32_e32 v16, 0
	v_mov_b32_e32 v17, 0
	v_mov_b32_e32 v40, 0
	v_mov_b32_e32 v47, 0x42fe0000
	s_mov_b32 s32, 0x42fe0000
	s_mov_b32 s33, 0xc0c0400
	s_mov_b32 s34, 0x4000c0c
	s_mov_b32 s15, s12
	s_mul_i32 s37, s15, 0xfa0
	s_lshl_b32 s15, s15, 7
	s_waitcnt lgkmcnt(0)
	s_add_u32 s16, s4, s37
	s_addc_u32 s17, s5, 0
	s_add_u32 s40, s6, s15
	s_addc_u32 s41, s7, 0
	s_add_u32 s20, s40, 0
	s_addc_u32 s21, s41, 0
	s_add_u32 s22, s20, 0x186a000
	s_addc_u32 s23, s21, 0
	s_add_u32 s24, s22, 0x186a000
	s_addc_u32 s25, s23, 0
	s_add_u32 s26, s24, 0x186a000
	s_addc_u32 s27, s25, 0
	s_mov_b32 m0, s35
	s_nop 0
	global_load_lds_dwordx4 v34, s[16:17] nt
	global_load_lds_dwordx4 v34, s[16:17] offset:1024 nt
	global_load_lds_dwordx4 v34, s[16:17] offset:2048 nt
	global_load_lds_dwordx4 v35, s[16:17] offset:3072 nt
	s_add_u32 s16, s16, 0xfa0000
	s_addc_u32 s17, s17, 0
	s_waitcnt vmcnt(0)
	ds_read_b128 v[18:21], v38 offset:0
	ds_read_b128 v[22:25], v38 offset:1024
	ds_read_b128 v[26:29], v38 offset:2048
	ds_read_b128 v[30:33], v38 offset:3072
	s_waitcnt lgkmcnt(0)
	s_barrier
	s_mov_b32 m0, s35
	s_nop 0
	global_load_lds_dwordx4 v34, s[16:17] nt
	global_load_lds_dwordx4 v34, s[16:17] offset:1024 nt
	global_load_lds_dwordx4 v34, s[16:17] offset:2048 nt
	global_load_lds_dwordx4 v35, s[16:17] offset:3072 nt
	s_add_u32 s16, s16, 0xfa0000
	s_addc_u32 s17, s17, 0
	v_cndmask_b32_e64 v30, 0, v30, s[18:19]
	v_cndmask_b32_e64 v31, 0, v31, s[18:19]
	v_cndmask_b32_e64 v32, 0, v32, s[18:19]
	v_cndmask_b32_e64 v33, 0, v33, s[18:19]
	v_max3_f32 v41, |v18|, |v19|, |v20|
	v_max3_f32 v42, |v21|, |v22|, |v23|
	v_max3_f32 v43, |v24|, |v25|, |v26|
	v_max3_f32 v44, |v27|, |v28|, |v29|
	v_max3_f32 v48, |v30|, |v31|, |v32|
	v_max3_f32 v41, v41, v42, |v33|
	v_max3_f32 v43, v43, v44, v48
	v_max_f32_e32 v41, v41, v43
	v_pk_add_f32 v[2:3], v[2:3], v[18:19]
	v_pk_add_f32 v[4:5], v[4:5], v[20:21]
	v_max_f32_dpp v41, v41, v41 quad_perm:[1,0,3,2] row_mask:0xf bank_mask:0xf
	v_pk_add_f32 v[6:7], v[6:7], v[22:23]
	v_pk_add_f32 v[8:9], v[8:9], v[24:25]
	v_max_f32_dpp v41, v41, v41 quad_perm:[2,3,0,1] row_mask:0xf bank_mask:0xf
	v_pk_add_f32 v[10:11], v[10:11], v[26:27]
	v_pk_add_f32 v[12:13], v[12:13], v[28:29]
	v_max_f32_dpp v41, v41, v41 row_half_mirror row_mask:0xf bank_mask:0xf
	v_pk_add_f32 v[14:15], v[14:15], v[30:31]
	v_pk_add_f32 v[16:17], v[16:17], v[32:33]
	v_max_f32_dpp v41, v41, v41 row_mirror row_mask:0xf bank_mask:0xf
	s_nop 1
	v_max_f32_dpp v41, v41, v41 row_bcast:15 row_mask:0xa bank_mask:0xf
	s_nop 1
	v_max_f32_dpp v41, v41, v41 row_bcast:31 row_mask:0xc bank_mask:0xf
	s_nop 1
	v_readlane_b32 s28, v41, 63
	s_nop 1
	v_div_scale_f32 v48, s[30:31], s28, s28, v47
	v_rcp_f32_e32 v49, v48
	s_nop 0
	v_fma_f32 v50, -v48, v49, 1.0
	v_fmac_f32_e32 v49, v50, v49
	v_mov_b32_e32 v50, s28
	v_div_scale_f32 v50, vcc, s32, v50, s32
	v_mul_f32_e32 v51, v50, v49
	v_fma_f32 v52, -v48, v51, v50
	v_fmac_f32_e32 v51, v52, v49
	v_fma_f32 v48, -v48, v51, v50
	v_div_fmas_f32 v48, v48, v49, v51
	v_div_fixup_f32 v48, v48, s28, v47
	v_cmp_gt_f32_e64 vcc, s28, 0
	v_writelane_b32 v40, s28, 0
	s_nop 0
	v_cndmask_b32_e32 v48, 0, v48, vcc
	v_fmaak_f32 v49, v18, v48, 0x4b400000
	v_fmaak_f32 v50, v19, v48, 0x4b400000
	v_fmaak_f32 v51, v20, v48, 0x4b400000
	v_fmaak_f32 v52, v21, v48, 0x4b400000
	v_perm_b32 v49, v50, v49, s33
	v_perm_b32 v51, v52, v51, s34
	v_or_b32_e32 v56, v49, v51
	v_fmaak_f32 v41, v22, v48, 0x4b400000
	v_fmaak_f32 v42, v23, v48, 0x4b400000
	v_fmaak_f32 v43, v24, v48, 0x4b400000
	v_fmaak_f32 v44, v25, v48, 0x4b400000
	v_perm_b32 v41, v42, v41, s33
	v_perm_b32 v43, v44, v43, s34
	v_or_b32_e32 v57, v41, v43
	v_fmaak_f32 v49, v26, v48, 0x4b400000
	v_fmaak_f32 v50, v27, v48, 0x4b400000
	v_fmaak_f32 v51, v28, v48, 0x4b400000
	v_fmaak_f32 v52, v29, v48, 0x4b400000
	v_perm_b32 v49, v50, v49, s33
	v_perm_b32 v51, v52, v51, s34
	v_or_b32_e32 v58, v49, v51
	v_fmaak_f32 v41, v30, v48, 0x4b400000
	v_fmaak_f32 v42, v31, v48, 0x4b400000
	v_fmaak_f32 v43, v32, v48, 0x4b400000
	v_fmaak_f32 v44, v33, v48, 0x4b400000
	v_perm_b32 v41, v42, v41, s33
	v_perm_b32 v43, v44, v43, s34
	v_or_b32_e32 v59, v41, v43
	s_waitcnt vmcnt(0)
	ds_read_b128 v[18:21], v38 offset:0
	ds_read_b128 v[22:25], v38 offset:1024
	ds_read_b128 v[26:29], v38 offset:2048
	ds_read_b128 v[30:33], v38 offset:3072
	s_waitcnt lgkmcnt(0)
	s_barrier
	s_mov_b32 m0, s35
	s_nop 0
	global_load_lds_dwordx4 v34, s[16:17] nt
	global_load_lds_dwordx4 v34, s[16:17] offset:1024 nt
	global_load_lds_dwordx4 v34, s[16:17] offset:2048 nt
	global_load_lds_dwordx4 v35, s[16:17] offset:3072 nt
	s_add_u32 s16, s16, 0xfa0000
	s_addc_u32 s17, s17, 0
	v_cndmask_b32_e64 v30, 0, v30, s[18:19]
	v_cndmask_b32_e64 v31, 0, v31, s[18:19]
	v_cndmask_b32_e64 v32, 0, v32, s[18:19]
	v_cndmask_b32_e64 v33, 0, v33, s[18:19]
	v_max3_f32 v41, |v18|, |v19|, |v20|
	v_max3_f32 v42, |v21|, |v22|, |v23|
	v_max3_f32 v43, |v24|, |v25|, |v26|
	v_max3_f32 v44, |v27|, |v28|, |v29|
	v_max3_f32 v48, |v30|, |v31|, |v32|
	v_max3_f32 v41, v41, v42, |v33|
	v_max3_f32 v43, v43, v44, v48
	v_max_f32_e32 v41, v41, v43
	v_pk_add_f32 v[2:3], v[2:3], v[18:19]
	v_pk_add_f32 v[4:5], v[4:5], v[20:21]
	v_max_f32_dpp v41, v41, v41 quad_perm:[1,0,3,2] row_mask:0xf bank_mask:0xf
	v_pk_add_f32 v[6:7], v[6:7], v[22:23]
	v_pk_add_f32 v[8:9], v[8:9], v[24:25]
	v_max_f32_dpp v41, v41, v41 quad_perm:[2,3,0,1] row_mask:0xf bank_mask:0xf
	v_pk_add_f32 v[10:11], v[10:11], v[26:27]
	v_pk_add_f32 v[12:13], v[12:13], v[28:29]
	v_max_f32_dpp v41, v41, v41 row_half_mirror row_mask:0xf bank_mask:0xf
	v_pk_add_f32 v[14:15], v[14:15], v[30:31]
	v_pk_add_f32 v[16:17], v[16:17], v[32:33]
	v_max_f32_dpp v41, v41, v41 row_mirror row_mask:0xf bank_mask:0xf
	s_nop 1
	v_max_f32_dpp v41, v41, v41 row_bcast:15 row_mask:0xa bank_mask:0xf
	s_nop 1
	v_max_f32_dpp v41, v41, v41 row_bcast:31 row_mask:0xc bank_mask:0xf
	s_nop 1
	v_readlane_b32 s28, v41, 63
	s_nop 1
	v_div_scale_f32 v48, s[30:31], s28, s28, v47
	v_rcp_f32_e32 v49, v48
	s_nop 0
	v_fma_f32 v50, -v48, v49, 1.0
	v_fmac_f32_e32 v49, v50, v49
	v_mov_b32_e32 v50, s28
	v_div_scale_f32 v50, vcc, s32, v50, s32
	v_mul_f32_e32 v51, v50, v49
	v_fma_f32 v52, -v48, v51, v50
	v_fmac_f32_e32 v51, v52, v49
	v_fma_f32 v48, -v48, v51, v50
	v_div_fmas_f32 v48, v48, v49, v51
	v_div_fixup_f32 v48, v48, s28, v47
	v_cmp_gt_f32_e64 vcc, s28, 0
	v_writelane_b32 v40, s28, 1
	s_nop 0
	v_cndmask_b32_e32 v48, 0, v48, vcc
	v_fmaak_f32 v49, v18, v48, 0x4b400000
	v_fmaak_f32 v50, v19, v48, 0x4b400000
	v_fmaak_f32 v51, v20, v48, 0x4b400000
	v_fmaak_f32 v52, v21, v48, 0x4b400000
	v_perm_b32 v49, v50, v49, s33
	v_perm_b32 v51, v52, v51, s34
	v_or_b32_e32 v60, v49, v51
	v_fmaak_f32 v41, v22, v48, 0x4b400000
	v_fmaak_f32 v42, v23, v48, 0x4b400000
	v_fmaak_f32 v43, v24, v48, 0x4b400000
	v_fmaak_f32 v44, v25, v48, 0x4b400000
	v_perm_b32 v41, v42, v41, s33
	v_perm_b32 v43, v44, v43, s34
	v_or_b32_e32 v61, v41, v43
	v_fmaak_f32 v49, v26, v48, 0x4b400000
	v_fmaak_f32 v50, v27, v48, 0x4b400000
	v_fmaak_f32 v51, v28, v48, 0x4b400000
	v_fmaak_f32 v52, v29, v48, 0x4b400000
	v_perm_b32 v49, v50, v49, s33
	v_perm_b32 v51, v52, v51, s34
	v_or_b32_e32 v62, v49, v51
	v_fmaak_f32 v41, v30, v48, 0x4b400000
	v_fmaak_f32 v42, v31, v48, 0x4b400000
	v_fmaak_f32 v43, v32, v48, 0x4b400000
	v_fmaak_f32 v44, v33, v48, 0x4b400000
	v_perm_b32 v41, v42, v41, s33
	v_perm_b32 v43, v44, v43, s34
	v_or_b32_e32 v63, v41, v43
	s_waitcnt vmcnt(0)
	ds_read_b128 v[18:21], v38 offset:0
	ds_read_b128 v[22:25], v38 offset:1024
	ds_read_b128 v[26:29], v38 offset:2048
	ds_read_b128 v[30:33], v38 offset:3072
	s_waitcnt lgkmcnt(0)
	s_barrier
	s_mov_b32 m0, s35
	s_nop 0
	global_load_lds_dwordx4 v34, s[16:17] nt
	global_load_lds_dwordx4 v34, s[16:17] offset:1024 nt
	global_load_lds_dwordx4 v34, s[16:17] offset:2048 nt
	global_load_lds_dwordx4 v35, s[16:17] offset:3072 nt
	s_add_u32 s16, s16, 0xfa0000
	s_addc_u32 s17, s17, 0
	v_cndmask_b32_e64 v30, 0, v30, s[18:19]
	v_cndmask_b32_e64 v31, 0, v31, s[18:19]
	v_cndmask_b32_e64 v32, 0, v32, s[18:19]
	v_cndmask_b32_e64 v33, 0, v33, s[18:19]
	v_max3_f32 v41, |v18|, |v19|, |v20|
	v_max3_f32 v42, |v21|, |v22|, |v23|
	v_max3_f32 v43, |v24|, |v25|, |v26|
	v_max3_f32 v44, |v27|, |v28|, |v29|
	v_max3_f32 v48, |v30|, |v31|, |v32|
	v_max3_f32 v41, v41, v42, |v33|
	v_max3_f32 v43, v43, v44, v48
	v_max_f32_e32 v41, v41, v43
	v_pk_add_f32 v[2:3], v[2:3], v[18:19]
	v_pk_add_f32 v[4:5], v[4:5], v[20:21]
	v_max_f32_dpp v41, v41, v41 quad_perm:[1,0,3,2] row_mask:0xf bank_mask:0xf
	v_pk_add_f32 v[6:7], v[6:7], v[22:23]
	v_pk_add_f32 v[8:9], v[8:9], v[24:25]
	v_max_f32_dpp v41, v41, v41 quad_perm:[2,3,0,1] row_mask:0xf bank_mask:0xf
	v_pk_add_f32 v[10:11], v[10:11], v[26:27]
	v_pk_add_f32 v[12:13], v[12:13], v[28:29]
	v_max_f32_dpp v41, v41, v41 row_half_mirror row_mask:0xf bank_mask:0xf
	v_pk_add_f32 v[14:15], v[14:15], v[30:31]
	v_pk_add_f32 v[16:17], v[16:17], v[32:33]
	v_max_f32_dpp v41, v41, v41 row_mirror row_mask:0xf bank_mask:0xf
	s_nop 1
	v_max_f32_dpp v41, v41, v41 row_bcast:15 row_mask:0xa bank_mask:0xf
	s_nop 1
	v_max_f32_dpp v41, v41, v41 row_bcast:31 row_mask:0xc bank_mask:0xf
	s_nop 1
	v_readlane_b32 s28, v41, 63
	s_nop 1
	v_div_scale_f32 v48, s[30:31], s28, s28, v47
	v_rcp_f32_e32 v49, v48
	s_nop 0
	v_fma_f32 v50, -v48, v49, 1.0
	v_fmac_f32_e32 v49, v50, v49
	v_mov_b32_e32 v50, s28
	v_div_scale_f32 v50, vcc, s32, v50, s32
	v_mul_f32_e32 v51, v50, v49
	v_fma_f32 v52, -v48, v51, v50
	v_fmac_f32_e32 v51, v52, v49
	v_fma_f32 v48, -v48, v51, v50
	v_div_fmas_f32 v48, v48, v49, v51
	v_div_fixup_f32 v48, v48, s28, v47
	v_cmp_gt_f32_e64 vcc, s28, 0
	v_writelane_b32 v40, s28, 2
	s_nop 0
	v_cndmask_b32_e32 v48, 0, v48, vcc
	v_fmaak_f32 v49, v18, v48, 0x4b400000
	v_fmaak_f32 v50, v19, v48, 0x4b400000
	v_fmaak_f32 v51, v20, v48, 0x4b400000
	v_fmaak_f32 v52, v21, v48, 0x4b400000
	v_perm_b32 v49, v50, v49, s33
	v_perm_b32 v51, v52, v51, s34
	v_or_b32_e32 v64, v49, v51
	v_fmaak_f32 v41, v22, v48, 0x4b400000
	v_fmaak_f32 v42, v23, v48, 0x4b400000
	v_fmaak_f32 v43, v24, v48, 0x4b400000
	v_fmaak_f32 v44, v25, v48, 0x4b400000
	v_perm_b32 v41, v42, v41, s33
	v_perm_b32 v43, v44, v43, s34
	v_or_b32_e32 v65, v41, v43
	v_fmaak_f32 v49, v26, v48, 0x4b400000
	v_fmaak_f32 v50, v27, v48, 0x4b400000
	v_fmaak_f32 v51, v28, v48, 0x4b400000
	v_fmaak_f32 v52, v29, v48, 0x4b400000
	v_perm_b32 v49, v50, v49, s33
	v_perm_b32 v51, v52, v51, s34
	v_or_b32_e32 v66, v49, v51
	v_fmaak_f32 v41, v30, v48, 0x4b400000
	v_fmaak_f32 v42, v31, v48, 0x4b400000
	v_fmaak_f32 v43, v32, v48, 0x4b400000
	v_fmaak_f32 v44, v33, v48, 0x4b400000
	v_perm_b32 v41, v42, v41, s33
	v_perm_b32 v43, v44, v43, s34
	v_or_b32_e32 v67, v41, v43
	s_waitcnt vmcnt(0)
	ds_read_b128 v[18:21], v38 offset:0
	ds_read_b128 v[22:25], v38 offset:1024
	ds_read_b128 v[26:29], v38 offset:2048
	ds_read_b128 v[30:33], v38 offset:3072
	s_waitcnt lgkmcnt(0)
	s_barrier
	s_mov_b32 m0, s35
	s_nop 0
	global_load_lds_dwordx4 v34, s[16:17] nt
	global_load_lds_dwordx4 v34, s[16:17] offset:1024 nt
	global_load_lds_dwordx4 v34, s[16:17] offset:2048 nt
	global_load_lds_dwordx4 v35, s[16:17] offset:3072 nt
	s_add_u32 s16, s16, 0xfa0000
	s_addc_u32 s17, s17, 0
	v_cndmask_b32_e64 v30, 0, v30, s[18:19]
	v_cndmask_b32_e64 v31, 0, v31, s[18:19]
	v_cndmask_b32_e64 v32, 0, v32, s[18:19]
	v_cndmask_b32_e64 v33, 0, v33, s[18:19]
	v_max3_f32 v41, |v18|, |v19|, |v20|
	v_max3_f32 v42, |v21|, |v22|, |v23|
	v_max3_f32 v43, |v24|, |v25|, |v26|
	v_max3_f32 v44, |v27|, |v28|, |v29|
	v_max3_f32 v48, |v30|, |v31|, |v32|
	v_max3_f32 v41, v41, v42, |v33|
	v_max3_f32 v43, v43, v44, v48
	v_max_f32_e32 v41, v41, v43
	v_pk_add_f32 v[2:3], v[2:3], v[18:19]
	v_pk_add_f32 v[4:5], v[4:5], v[20:21]
	v_max_f32_dpp v41, v41, v41 quad_perm:[1,0,3,2] row_mask:0xf bank_mask:0xf
	v_pk_add_f32 v[6:7], v[6:7], v[22:23]
	v_pk_add_f32 v[8:9], v[8:9], v[24:25]
	v_max_f32_dpp v41, v41, v41 quad_perm:[2,3,0,1] row_mask:0xf bank_mask:0xf
	v_pk_add_f32 v[10:11], v[10:11], v[26:27]
	v_pk_add_f32 v[12:13], v[12:13], v[28:29]
	v_max_f32_dpp v41, v41, v41 row_half_mirror row_mask:0xf bank_mask:0xf
	v_pk_add_f32 v[14:15], v[14:15], v[30:31]
	v_pk_add_f32 v[16:17], v[16:17], v[32:33]
	v_max_f32_dpp v41, v41, v41 row_mirror row_mask:0xf bank_mask:0xf
	s_nop 1
	v_max_f32_dpp v41, v41, v41 row_bcast:15 row_mask:0xa bank_mask:0xf
	s_nop 1
	v_max_f32_dpp v41, v41, v41 row_bcast:31 row_mask:0xc bank_mask:0xf
	s_nop 1
	v_readlane_b32 s28, v41, 63
	s_nop 1
	v_div_scale_f32 v48, s[30:31], s28, s28, v47
	v_rcp_f32_e32 v49, v48
	s_nop 0
	v_fma_f32 v50, -v48, v49, 1.0
	v_fmac_f32_e32 v49, v50, v49
	v_mov_b32_e32 v50, s28
	v_div_scale_f32 v50, vcc, s32, v50, s32
	v_mul_f32_e32 v51, v50, v49
	v_fma_f32 v52, -v48, v51, v50
	v_fmac_f32_e32 v51, v52, v49
	v_fma_f32 v48, -v48, v51, v50
	v_div_fmas_f32 v48, v48, v49, v51
	v_div_fixup_f32 v48, v48, s28, v47
	v_cmp_gt_f32_e64 vcc, s28, 0
	v_writelane_b32 v40, s28, 3
	s_nop 0
	v_cndmask_b32_e32 v48, 0, v48, vcc
	v_fmaak_f32 v49, v18, v48, 0x4b400000
	v_fmaak_f32 v50, v19, v48, 0x4b400000
	v_fmaak_f32 v51, v20, v48, 0x4b400000
	v_fmaak_f32 v52, v21, v48, 0x4b400000
	v_perm_b32 v49, v50, v49, s33
	v_perm_b32 v51, v52, v51, s34
	v_or_b32_e32 v68, v49, v51
	v_fmaak_f32 v41, v22, v48, 0x4b400000
	v_fmaak_f32 v42, v23, v48, 0x4b400000
	v_fmaak_f32 v43, v24, v48, 0x4b400000
	v_fmaak_f32 v44, v25, v48, 0x4b400000
	v_perm_b32 v41, v42, v41, s33
	v_perm_b32 v43, v44, v43, s34
	v_or_b32_e32 v69, v41, v43
	v_fmaak_f32 v49, v26, v48, 0x4b400000
	v_fmaak_f32 v50, v27, v48, 0x4b400000
	v_fmaak_f32 v51, v28, v48, 0x4b400000
	v_fmaak_f32 v52, v29, v48, 0x4b400000
	v_perm_b32 v49, v50, v49, s33
	v_perm_b32 v51, v52, v51, s34
	v_or_b32_e32 v70, v49, v51
	v_fmaak_f32 v41, v30, v48, 0x4b400000
	v_fmaak_f32 v42, v31, v48, 0x4b400000
	v_fmaak_f32 v43, v32, v48, 0x4b400000
	v_fmaak_f32 v44, v33, v48, 0x4b400000
	v_perm_b32 v41, v42, v41, s33
	v_perm_b32 v43, v44, v43, s34
	v_or_b32_e32 v71, v41, v43
	s_waitcnt vmcnt(0)
	ds_read_b128 v[18:21], v38 offset:0
	ds_read_b128 v[22:25], v38 offset:1024
	ds_read_b128 v[26:29], v38 offset:2048
	ds_read_b128 v[30:33], v38 offset:3072
	s_waitcnt lgkmcnt(0)
	s_barrier
	s_mov_b32 m0, s35
	s_nop 0
	global_load_lds_dwordx4 v34, s[16:17] nt
	global_load_lds_dwordx4 v34, s[16:17] offset:1024 nt
	global_load_lds_dwordx4 v34, s[16:17] offset:2048 nt
	global_load_lds_dwordx4 v35, s[16:17] offset:3072 nt
	s_add_u32 s16, s16, 0xfa0000
	s_addc_u32 s17, s17, 0
	v_cndmask_b32_e64 v30, 0, v30, s[18:19]
	v_cndmask_b32_e64 v31, 0, v31, s[18:19]
	v_cndmask_b32_e64 v32, 0, v32, s[18:19]
	v_cndmask_b32_e64 v33, 0, v33, s[18:19]
	v_max3_f32 v41, |v18|, |v19|, |v20|
	v_max3_f32 v42, |v21|, |v22|, |v23|
	v_max3_f32 v43, |v24|, |v25|, |v26|
	v_max3_f32 v44, |v27|, |v28|, |v29|
	v_max3_f32 v48, |v30|, |v31|, |v32|
	v_max3_f32 v41, v41, v42, |v33|
	v_max3_f32 v43, v43, v44, v48
	v_max_f32_e32 v41, v41, v43
	v_pk_add_f32 v[2:3], v[2:3], v[18:19]
	v_pk_add_f32 v[4:5], v[4:5], v[20:21]
	v_max_f32_dpp v41, v41, v41 quad_perm:[1,0,3,2] row_mask:0xf bank_mask:0xf
	v_pk_add_f32 v[6:7], v[6:7], v[22:23]
	v_pk_add_f32 v[8:9], v[8:9], v[24:25]
	v_max_f32_dpp v41, v41, v41 quad_perm:[2,3,0,1] row_mask:0xf bank_mask:0xf
	v_pk_add_f32 v[10:11], v[10:11], v[26:27]
	v_pk_add_f32 v[12:13], v[12:13], v[28:29]
	v_max_f32_dpp v41, v41, v41 row_half_mirror row_mask:0xf bank_mask:0xf
	v_pk_add_f32 v[14:15], v[14:15], v[30:31]
	v_pk_add_f32 v[16:17], v[16:17], v[32:33]
	v_max_f32_dpp v41, v41, v41 row_mirror row_mask:0xf bank_mask:0xf
	s_nop 1
	v_max_f32_dpp v41, v41, v41 row_bcast:15 row_mask:0xa bank_mask:0xf
	s_nop 1
	v_max_f32_dpp v41, v41, v41 row_bcast:31 row_mask:0xc bank_mask:0xf
	s_nop 1
	v_readlane_b32 s28, v41, 63
	s_nop 1
	v_div_scale_f32 v48, s[30:31], s28, s28, v47
	v_rcp_f32_e32 v49, v48
	s_nop 0
	v_fma_f32 v50, -v48, v49, 1.0
	v_fmac_f32_e32 v49, v50, v49
	v_mov_b32_e32 v50, s28
	v_div_scale_f32 v50, vcc, s32, v50, s32
	v_mul_f32_e32 v51, v50, v49
	v_fma_f32 v52, -v48, v51, v50
	v_fmac_f32_e32 v51, v52, v49
	v_fma_f32 v48, -v48, v51, v50
	v_div_fmas_f32 v48, v48, v49, v51
	v_div_fixup_f32 v48, v48, s28, v47
	v_cmp_gt_f32_e64 vcc, s28, 0
	v_writelane_b32 v40, s28, 4
	s_nop 0
	v_cndmask_b32_e32 v48, 0, v48, vcc
	v_fmaak_f32 v49, v18, v48, 0x4b400000
	v_fmaak_f32 v50, v19, v48, 0x4b400000
	v_fmaak_f32 v51, v20, v48, 0x4b400000
	v_fmaak_f32 v52, v21, v48, 0x4b400000
	v_perm_b32 v49, v50, v49, s33
	v_perm_b32 v51, v52, v51, s34
	v_or_b32_e32 v72, v49, v51
	v_fmaak_f32 v41, v22, v48, 0x4b400000
	v_fmaak_f32 v42, v23, v48, 0x4b400000
	v_fmaak_f32 v43, v24, v48, 0x4b400000
	v_fmaak_f32 v44, v25, v48, 0x4b400000
	v_perm_b32 v41, v42, v41, s33
	v_perm_b32 v43, v44, v43, s34
	v_or_b32_e32 v73, v41, v43
	v_fmaak_f32 v49, v26, v48, 0x4b400000
	v_fmaak_f32 v50, v27, v48, 0x4b400000
	v_fmaak_f32 v51, v28, v48, 0x4b400000
	v_fmaak_f32 v52, v29, v48, 0x4b400000
	v_perm_b32 v49, v50, v49, s33
	v_perm_b32 v51, v52, v51, s34
	v_or_b32_e32 v74, v49, v51
	v_fmaak_f32 v41, v30, v48, 0x4b400000
	v_fmaak_f32 v42, v31, v48, 0x4b400000
	v_fmaak_f32 v43, v32, v48, 0x4b400000
	v_fmaak_f32 v44, v33, v48, 0x4b400000
	v_perm_b32 v41, v42, v41, s33
	v_perm_b32 v43, v44, v43, s34
	v_or_b32_e32 v75, v41, v43
	s_waitcnt vmcnt(0)
	ds_read_b128 v[18:21], v38 offset:0
	ds_read_b128 v[22:25], v38 offset:1024
	ds_read_b128 v[26:29], v38 offset:2048
	ds_read_b128 v[30:33], v38 offset:3072
	s_waitcnt lgkmcnt(0)
	s_barrier
	s_mov_b32 m0, s35
	s_nop 0
	global_load_lds_dwordx4 v34, s[16:17] nt
	global_load_lds_dwordx4 v34, s[16:17] offset:1024 nt
	global_load_lds_dwordx4 v34, s[16:17] offset:2048 nt
	global_load_lds_dwordx4 v35, s[16:17] offset:3072 nt
	s_add_u32 s16, s16, 0xfa0000
	s_addc_u32 s17, s17, 0
	v_cndmask_b32_e64 v30, 0, v30, s[18:19]
	v_cndmask_b32_e64 v31, 0, v31, s[18:19]
	v_cndmask_b32_e64 v32, 0, v32, s[18:19]
	v_cndmask_b32_e64 v33, 0, v33, s[18:19]
	v_max3_f32 v41, |v18|, |v19|, |v20|
	v_max3_f32 v42, |v21|, |v22|, |v23|
	v_max3_f32 v43, |v24|, |v25|, |v26|
	v_max3_f32 v44, |v27|, |v28|, |v29|
	v_max3_f32 v48, |v30|, |v31|, |v32|
	v_max3_f32 v41, v41, v42, |v33|
	v_max3_f32 v43, v43, v44, v48
	v_max_f32_e32 v41, v41, v43
	v_pk_add_f32 v[2:3], v[2:3], v[18:19]
	v_pk_add_f32 v[4:5], v[4:5], v[20:21]
	v_max_f32_dpp v41, v41, v41 quad_perm:[1,0,3,2] row_mask:0xf bank_mask:0xf
	v_pk_add_f32 v[6:7], v[6:7], v[22:23]
	v_pk_add_f32 v[8:9], v[8:9], v[24:25]
	v_max_f32_dpp v41, v41, v41 quad_perm:[2,3,0,1] row_mask:0xf bank_mask:0xf
	v_pk_add_f32 v[10:11], v[10:11], v[26:27]
	v_pk_add_f32 v[12:13], v[12:13], v[28:29]
	v_max_f32_dpp v41, v41, v41 row_half_mirror row_mask:0xf bank_mask:0xf
	v_pk_add_f32 v[14:15], v[14:15], v[30:31]
	v_pk_add_f32 v[16:17], v[16:17], v[32:33]
	v_max_f32_dpp v41, v41, v41 row_mirror row_mask:0xf bank_mask:0xf
	s_nop 1
	v_max_f32_dpp v41, v41, v41 row_bcast:15 row_mask:0xa bank_mask:0xf
	s_nop 1
	v_max_f32_dpp v41, v41, v41 row_bcast:31 row_mask:0xc bank_mask:0xf
	s_nop 1
	v_readlane_b32 s28, v41, 63
	s_nop 1
	v_div_scale_f32 v48, s[30:31], s28, s28, v47
	v_rcp_f32_e32 v49, v48
	s_nop 0
	v_fma_f32 v50, -v48, v49, 1.0
	v_fmac_f32_e32 v49, v50, v49
	v_mov_b32_e32 v50, s28
	v_div_scale_f32 v50, vcc, s32, v50, s32
	v_mul_f32_e32 v51, v50, v49
	v_fma_f32 v52, -v48, v51, v50
	v_fmac_f32_e32 v51, v52, v49
	v_fma_f32 v48, -v48, v51, v50
	v_div_fmas_f32 v48, v48, v49, v51
	v_div_fixup_f32 v48, v48, s28, v47
	v_cmp_gt_f32_e64 vcc, s28, 0
	v_writelane_b32 v40, s28, 5
	s_nop 0
	v_cndmask_b32_e32 v48, 0, v48, vcc
	v_fmaak_f32 v49, v18, v48, 0x4b400000
	v_fmaak_f32 v50, v19, v48, 0x4b400000
	v_fmaak_f32 v51, v20, v48, 0x4b400000
	v_fmaak_f32 v52, v21, v48, 0x4b400000
	v_perm_b32 v49, v50, v49, s33
	v_perm_b32 v51, v52, v51, s34
	v_or_b32_e32 v76, v49, v51
	v_fmaak_f32 v41, v22, v48, 0x4b400000
	v_fmaak_f32 v42, v23, v48, 0x4b400000
	v_fmaak_f32 v43, v24, v48, 0x4b400000
	v_fmaak_f32 v44, v25, v48, 0x4b400000
	v_perm_b32 v41, v42, v41, s33
	v_perm_b32 v43, v44, v43, s34
	v_or_b32_e32 v77, v41, v43
	v_fmaak_f32 v49, v26, v48, 0x4b400000
	v_fmaak_f32 v50, v27, v48, 0x4b400000
	v_fmaak_f32 v51, v28, v48, 0x4b400000
	v_fmaak_f32 v52, v29, v48, 0x4b400000
	v_perm_b32 v49, v50, v49, s33
	v_perm_b32 v51, v52, v51, s34
	v_or_b32_e32 v78, v49, v51
	v_fmaak_f32 v41, v30, v48, 0x4b400000
	v_fmaak_f32 v42, v31, v48, 0x4b400000
	v_fmaak_f32 v43, v32, v48, 0x4b400000
	v_fmaak_f32 v44, v33, v48, 0x4b400000
	v_perm_b32 v41, v42, v41, s33
	v_perm_b32 v43, v44, v43, s34
	v_or_b32_e32 v79, v41, v43
	s_waitcnt vmcnt(0)
	ds_read_b128 v[18:21], v38 offset:0
	ds_read_b128 v[22:25], v38 offset:1024
	ds_read_b128 v[26:29], v38 offset:2048
	ds_read_b128 v[30:33], v38 offset:3072
	s_waitcnt lgkmcnt(0)
	s_barrier
	s_mov_b32 m0, s35
	s_nop 0
	global_load_lds_dwordx4 v34, s[16:17] nt
	global_load_lds_dwordx4 v34, s[16:17] offset:1024 nt
	global_load_lds_dwordx4 v34, s[16:17] offset:2048 nt
	global_load_lds_dwordx4 v35, s[16:17] offset:3072 nt
	s_add_u32 s16, s16, 0xfa0000
	s_addc_u32 s17, s17, 0
	v_cndmask_b32_e64 v30, 0, v30, s[18:19]
	v_cndmask_b32_e64 v31, 0, v31, s[18:19]
	v_cndmask_b32_e64 v32, 0, v32, s[18:19]
	v_cndmask_b32_e64 v33, 0, v33, s[18:19]
	v_max3_f32 v41, |v18|, |v19|, |v20|
	v_max3_f32 v42, |v21|, |v22|, |v23|
	v_max3_f32 v43, |v24|, |v25|, |v26|
	v_max3_f32 v44, |v27|, |v28|, |v29|
	v_max3_f32 v48, |v30|, |v31|, |v32|
	v_max3_f32 v41, v41, v42, |v33|
	v_max3_f32 v43, v43, v44, v48
	v_max_f32_e32 v41, v41, v43
	v_pk_add_f32 v[2:3], v[2:3], v[18:19]
	v_pk_add_f32 v[4:5], v[4:5], v[20:21]
	v_max_f32_dpp v41, v41, v41 quad_perm:[1,0,3,2] row_mask:0xf bank_mask:0xf
	v_pk_add_f32 v[6:7], v[6:7], v[22:23]
	v_pk_add_f32 v[8:9], v[8:9], v[24:25]
	v_max_f32_dpp v41, v41, v41 quad_perm:[2,3,0,1] row_mask:0xf bank_mask:0xf
	v_pk_add_f32 v[10:11], v[10:11], v[26:27]
	v_pk_add_f32 v[12:13], v[12:13], v[28:29]
	v_max_f32_dpp v41, v41, v41 row_half_mirror row_mask:0xf bank_mask:0xf
	v_pk_add_f32 v[14:15], v[14:15], v[30:31]
	v_pk_add_f32 v[16:17], v[16:17], v[32:33]
	v_max_f32_dpp v41, v41, v41 row_mirror row_mask:0xf bank_mask:0xf
	s_nop 1
	v_max_f32_dpp v41, v41, v41 row_bcast:15 row_mask:0xa bank_mask:0xf
	s_nop 1
	v_max_f32_dpp v41, v41, v41 row_bcast:31 row_mask:0xc bank_mask:0xf
	s_nop 1
	v_readlane_b32 s28, v41, 63
	s_nop 1
	v_div_scale_f32 v48, s[30:31], s28, s28, v47
	v_rcp_f32_e32 v49, v48
	s_nop 0
	v_fma_f32 v50, -v48, v49, 1.0
	v_fmac_f32_e32 v49, v50, v49
	v_mov_b32_e32 v50, s28
	v_div_scale_f32 v50, vcc, s32, v50, s32
	v_mul_f32_e32 v51, v50, v49
	v_fma_f32 v52, -v48, v51, v50
	v_fmac_f32_e32 v51, v52, v49
	v_fma_f32 v48, -v48, v51, v50
	v_div_fmas_f32 v48, v48, v49, v51
	v_div_fixup_f32 v48, v48, s28, v47
	v_cmp_gt_f32_e64 vcc, s28, 0
	v_writelane_b32 v40, s28, 6
	s_nop 0
	v_cndmask_b32_e32 v48, 0, v48, vcc
	v_fmaak_f32 v49, v18, v48, 0x4b400000
	v_fmaak_f32 v50, v19, v48, 0x4b400000
	v_fmaak_f32 v51, v20, v48, 0x4b400000
	v_fmaak_f32 v52, v21, v48, 0x4b400000
	v_perm_b32 v49, v50, v49, s33
	v_perm_b32 v51, v52, v51, s34
	v_or_b32_e32 v80, v49, v51
	v_fmaak_f32 v41, v22, v48, 0x4b400000
	v_fmaak_f32 v42, v23, v48, 0x4b400000
	v_fmaak_f32 v43, v24, v48, 0x4b400000
	v_fmaak_f32 v44, v25, v48, 0x4b400000
	v_perm_b32 v41, v42, v41, s33
	v_perm_b32 v43, v44, v43, s34
	v_or_b32_e32 v81, v41, v43
	v_fmaak_f32 v49, v26, v48, 0x4b400000
	v_fmaak_f32 v50, v27, v48, 0x4b400000
	v_fmaak_f32 v51, v28, v48, 0x4b400000
	v_fmaak_f32 v52, v29, v48, 0x4b400000
	v_perm_b32 v49, v50, v49, s33
	v_perm_b32 v51, v52, v51, s34
	v_or_b32_e32 v82, v49, v51
	v_fmaak_f32 v41, v30, v48, 0x4b400000
	v_fmaak_f32 v42, v31, v48, 0x4b400000
	v_fmaak_f32 v43, v32, v48, 0x4b400000
	v_fmaak_f32 v44, v33, v48, 0x4b400000
	v_perm_b32 v41, v42, v41, s33
	v_perm_b32 v43, v44, v43, s34
	v_or_b32_e32 v83, v41, v43
	s_waitcnt vmcnt(0)
	ds_read_b128 v[18:21], v38 offset:0
	ds_read_b128 v[22:25], v38 offset:1024
	ds_read_b128 v[26:29], v38 offset:2048
	ds_read_b128 v[30:33], v38 offset:3072
	s_waitcnt lgkmcnt(0)
	s_barrier
	s_mov_b32 m0, s35
	s_nop 0
	global_load_lds_dwordx4 v34, s[16:17] nt
	global_load_lds_dwordx4 v34, s[16:17] offset:1024 nt
	global_load_lds_dwordx4 v34, s[16:17] offset:2048 nt
	global_load_lds_dwordx4 v35, s[16:17] offset:3072 nt
	s_add_u32 s16, s16, 0xfa0000
	s_addc_u32 s17, s17, 0
	v_cndmask_b32_e64 v30, 0, v30, s[18:19]
	v_cndmask_b32_e64 v31, 0, v31, s[18:19]
	v_cndmask_b32_e64 v32, 0, v32, s[18:19]
	v_cndmask_b32_e64 v33, 0, v33, s[18:19]
	v_max3_f32 v41, |v18|, |v19|, |v20|
	v_max3_f32 v42, |v21|, |v22|, |v23|
	v_max3_f32 v43, |v24|, |v25|, |v26|
	v_max3_f32 v44, |v27|, |v28|, |v29|
	v_max3_f32 v48, |v30|, |v31|, |v32|
	v_max3_f32 v41, v41, v42, |v33|
	v_max3_f32 v43, v43, v44, v48
	v_max_f32_e32 v41, v41, v43
	v_pk_add_f32 v[2:3], v[2:3], v[18:19]
	v_pk_add_f32 v[4:5], v[4:5], v[20:21]
	v_max_f32_dpp v41, v41, v41 quad_perm:[1,0,3,2] row_mask:0xf bank_mask:0xf
	v_pk_add_f32 v[6:7], v[6:7], v[22:23]
	v_pk_add_f32 v[8:9], v[8:9], v[24:25]
	v_max_f32_dpp v41, v41, v41 quad_perm:[2,3,0,1] row_mask:0xf bank_mask:0xf
	v_pk_add_f32 v[10:11], v[10:11], v[26:27]
	v_pk_add_f32 v[12:13], v[12:13], v[28:29]
	v_max_f32_dpp v41, v41, v41 row_half_mirror row_mask:0xf bank_mask:0xf
	v_pk_add_f32 v[14:15], v[14:15], v[30:31]
	v_pk_add_f32 v[16:17], v[16:17], v[32:33]
	v_max_f32_dpp v41, v41, v41 row_mirror row_mask:0xf bank_mask:0xf
	s_nop 1
	v_max_f32_dpp v41, v41, v41 row_bcast:15 row_mask:0xa bank_mask:0xf
	s_nop 1
	v_max_f32_dpp v41, v41, v41 row_bcast:31 row_mask:0xc bank_mask:0xf
	s_nop 1
	v_readlane_b32 s28, v41, 63
	s_nop 1
	v_div_scale_f32 v48, s[30:31], s28, s28, v47
	v_rcp_f32_e32 v49, v48
	s_nop 0
	v_fma_f32 v50, -v48, v49, 1.0
	v_fmac_f32_e32 v49, v50, v49
	v_mov_b32_e32 v50, s28
	v_div_scale_f32 v50, vcc, s32, v50, s32
	v_mul_f32_e32 v51, v50, v49
	v_fma_f32 v52, -v48, v51, v50
	v_fmac_f32_e32 v51, v52, v49
	v_fma_f32 v48, -v48, v51, v50
	v_div_fmas_f32 v48, v48, v49, v51
	v_div_fixup_f32 v48, v48, s28, v47
	v_cmp_gt_f32_e64 vcc, s28, 0
	v_writelane_b32 v40, s28, 7
	s_nop 0
	v_cndmask_b32_e32 v48, 0, v48, vcc
	v_fmaak_f32 v49, v18, v48, 0x4b400000
	v_fmaak_f32 v50, v19, v48, 0x4b400000
	v_fmaak_f32 v51, v20, v48, 0x4b400000
	v_fmaak_f32 v52, v21, v48, 0x4b400000
	v_perm_b32 v49, v50, v49, s33
	v_perm_b32 v51, v52, v51, s34
	v_or_b32_e32 v84, v49, v51
	v_fmaak_f32 v41, v22, v48, 0x4b400000
	v_fmaak_f32 v42, v23, v48, 0x4b400000
	v_fmaak_f32 v43, v24, v48, 0x4b400000
	v_fmaak_f32 v44, v25, v48, 0x4b400000
	v_perm_b32 v41, v42, v41, s33
	v_perm_b32 v43, v44, v43, s34
	v_or_b32_e32 v85, v41, v43
	v_fmaak_f32 v49, v26, v48, 0x4b400000
	v_fmaak_f32 v50, v27, v48, 0x4b400000
	v_fmaak_f32 v51, v28, v48, 0x4b400000
	v_fmaak_f32 v52, v29, v48, 0x4b400000
	v_perm_b32 v49, v50, v49, s33
	v_perm_b32 v51, v52, v51, s34
	v_or_b32_e32 v86, v49, v51
	v_fmaak_f32 v41, v30, v48, 0x4b400000
	v_fmaak_f32 v42, v31, v48, 0x4b400000
	v_fmaak_f32 v43, v32, v48, 0x4b400000
	v_fmaak_f32 v44, v33, v48, 0x4b400000
	v_perm_b32 v41, v42, v41, s33
	v_perm_b32 v43, v44, v43, s34
	v_or_b32_e32 v87, v41, v43
	s_waitcnt vmcnt(0)
	ds_read_b128 v[18:21], v38 offset:0
	ds_read_b128 v[22:25], v38 offset:1024
	ds_read_b128 v[26:29], v38 offset:2048
	ds_read_b128 v[30:33], v38 offset:3072
	s_waitcnt lgkmcnt(0)
	s_barrier
	s_mov_b32 m0, s35
	s_nop 0
	global_load_lds_dwordx4 v34, s[16:17] nt
	global_load_lds_dwordx4 v34, s[16:17] offset:1024 nt
	global_load_lds_dwordx4 v34, s[16:17] offset:2048 nt
	global_load_lds_dwordx4 v35, s[16:17] offset:3072 nt
	s_add_u32 s16, s16, 0xfa0000
	s_addc_u32 s17, s17, 0
	v_cndmask_b32_e64 v30, 0, v30, s[18:19]
	v_cndmask_b32_e64 v31, 0, v31, s[18:19]
	v_cndmask_b32_e64 v32, 0, v32, s[18:19]
	v_cndmask_b32_e64 v33, 0, v33, s[18:19]
	v_max3_f32 v41, |v18|, |v19|, |v20|
	v_max3_f32 v42, |v21|, |v22|, |v23|
	v_max3_f32 v43, |v24|, |v25|, |v26|
	v_max3_f32 v44, |v27|, |v28|, |v29|
	v_max3_f32 v48, |v30|, |v31|, |v32|
	v_max3_f32 v41, v41, v42, |v33|
	v_max3_f32 v43, v43, v44, v48
	v_max_f32_e32 v41, v41, v43
	v_pk_add_f32 v[2:3], v[2:3], v[18:19]
	v_pk_add_f32 v[4:5], v[4:5], v[20:21]
	v_max_f32_dpp v41, v41, v41 quad_perm:[1,0,3,2] row_mask:0xf bank_mask:0xf
	v_pk_add_f32 v[6:7], v[6:7], v[22:23]
	v_pk_add_f32 v[8:9], v[8:9], v[24:25]
	v_max_f32_dpp v41, v41, v41 quad_perm:[2,3,0,1] row_mask:0xf bank_mask:0xf
	v_pk_add_f32 v[10:11], v[10:11], v[26:27]
	v_pk_add_f32 v[12:13], v[12:13], v[28:29]
	v_max_f32_dpp v41, v41, v41 row_half_mirror row_mask:0xf bank_mask:0xf
	v_pk_add_f32 v[14:15], v[14:15], v[30:31]
	v_pk_add_f32 v[16:17], v[16:17], v[32:33]
	v_max_f32_dpp v41, v41, v41 row_mirror row_mask:0xf bank_mask:0xf
	s_nop 1
	v_max_f32_dpp v41, v41, v41 row_bcast:15 row_mask:0xa bank_mask:0xf
	s_nop 1
	v_max_f32_dpp v41, v41, v41 row_bcast:31 row_mask:0xc bank_mask:0xf
	s_nop 1
	v_readlane_b32 s28, v41, 63
	s_nop 1
	v_div_scale_f32 v48, s[30:31], s28, s28, v47
	v_rcp_f32_e32 v49, v48
	s_nop 0
	v_fma_f32 v50, -v48, v49, 1.0
	v_fmac_f32_e32 v49, v50, v49
	v_mov_b32_e32 v50, s28
	v_div_scale_f32 v50, vcc, s32, v50, s32
	v_mul_f32_e32 v51, v50, v49
	v_fma_f32 v52, -v48, v51, v50
	v_fmac_f32_e32 v51, v52, v49
	v_fma_f32 v48, -v48, v51, v50
	v_div_fmas_f32 v48, v48, v49, v51
	v_div_fixup_f32 v48, v48, s28, v47
	v_cmp_gt_f32_e64 vcc, s28, 0
	v_writelane_b32 v40, s28, 8
	s_nop 0
	v_cndmask_b32_e32 v48, 0, v48, vcc
	v_fmaak_f32 v49, v18, v48, 0x4b400000
	v_fmaak_f32 v50, v19, v48, 0x4b400000
	v_fmaak_f32 v51, v20, v48, 0x4b400000
	v_fmaak_f32 v52, v21, v48, 0x4b400000
	v_perm_b32 v49, v50, v49, s33
	v_perm_b32 v51, v52, v51, s34
	v_or_b32_e32 v88, v49, v51
	v_fmaak_f32 v41, v22, v48, 0x4b400000
	v_fmaak_f32 v42, v23, v48, 0x4b400000
	v_fmaak_f32 v43, v24, v48, 0x4b400000
	v_fmaak_f32 v44, v25, v48, 0x4b400000
	v_perm_b32 v41, v42, v41, s33
	v_perm_b32 v43, v44, v43, s34
	v_or_b32_e32 v89, v41, v43
	v_fmaak_f32 v49, v26, v48, 0x4b400000
	v_fmaak_f32 v50, v27, v48, 0x4b400000
	v_fmaak_f32 v51, v28, v48, 0x4b400000
	v_fmaak_f32 v52, v29, v48, 0x4b400000
	v_perm_b32 v49, v50, v49, s33
	v_perm_b32 v51, v52, v51, s34
	v_or_b32_e32 v90, v49, v51
	v_fmaak_f32 v41, v30, v48, 0x4b400000
	v_fmaak_f32 v42, v31, v48, 0x4b400000
	v_fmaak_f32 v43, v32, v48, 0x4b400000
	v_fmaak_f32 v44, v33, v48, 0x4b400000
	v_perm_b32 v41, v42, v41, s33
	v_perm_b32 v43, v44, v43, s34
	v_or_b32_e32 v91, v41, v43
	s_waitcnt vmcnt(0)
	ds_read_b128 v[18:21], v38 offset:0
	ds_read_b128 v[22:25], v38 offset:1024
	ds_read_b128 v[26:29], v38 offset:2048
	ds_read_b128 v[30:33], v38 offset:3072
	s_waitcnt lgkmcnt(0)
	s_barrier
	s_mov_b32 m0, s35
	s_nop 0
	global_load_lds_dwordx4 v34, s[16:17] nt
	global_load_lds_dwordx4 v34, s[16:17] offset:1024 nt
	global_load_lds_dwordx4 v34, s[16:17] offset:2048 nt
	global_load_lds_dwordx4 v35, s[16:17] offset:3072 nt
	s_add_u32 s16, s16, 0xfa0000
	s_addc_u32 s17, s17, 0
	v_cndmask_b32_e64 v30, 0, v30, s[18:19]
	v_cndmask_b32_e64 v31, 0, v31, s[18:19]
	v_cndmask_b32_e64 v32, 0, v32, s[18:19]
	v_cndmask_b32_e64 v33, 0, v33, s[18:19]
	v_max3_f32 v41, |v18|, |v19|, |v20|
	v_max3_f32 v42, |v21|, |v22|, |v23|
	v_max3_f32 v43, |v24|, |v25|, |v26|
	v_max3_f32 v44, |v27|, |v28|, |v29|
	v_max3_f32 v48, |v30|, |v31|, |v32|
	v_max3_f32 v41, v41, v42, |v33|
	v_max3_f32 v43, v43, v44, v48
	v_max_f32_e32 v41, v41, v43
	v_pk_add_f32 v[2:3], v[2:3], v[18:19]
	v_pk_add_f32 v[4:5], v[4:5], v[20:21]
	v_max_f32_dpp v41, v41, v41 quad_perm:[1,0,3,2] row_mask:0xf bank_mask:0xf
	v_pk_add_f32 v[6:7], v[6:7], v[22:23]
	v_pk_add_f32 v[8:9], v[8:9], v[24:25]
	v_max_f32_dpp v41, v41, v41 quad_perm:[2,3,0,1] row_mask:0xf bank_mask:0xf
	v_pk_add_f32 v[10:11], v[10:11], v[26:27]
	v_pk_add_f32 v[12:13], v[12:13], v[28:29]
	v_max_f32_dpp v41, v41, v41 row_half_mirror row_mask:0xf bank_mask:0xf
	v_pk_add_f32 v[14:15], v[14:15], v[30:31]
	v_pk_add_f32 v[16:17], v[16:17], v[32:33]
	v_max_f32_dpp v41, v41, v41 row_mirror row_mask:0xf bank_mask:0xf
	s_nop 1
	v_max_f32_dpp v41, v41, v41 row_bcast:15 row_mask:0xa bank_mask:0xf
	s_nop 1
	v_max_f32_dpp v41, v41, v41 row_bcast:31 row_mask:0xc bank_mask:0xf
	s_nop 1
	v_readlane_b32 s28, v41, 63
	s_nop 1
	v_div_scale_f32 v48, s[30:31], s28, s28, v47
	v_rcp_f32_e32 v49, v48
	s_nop 0
	v_fma_f32 v50, -v48, v49, 1.0
	v_fmac_f32_e32 v49, v50, v49
	v_mov_b32_e32 v50, s28
	v_div_scale_f32 v50, vcc, s32, v50, s32
	v_mul_f32_e32 v51, v50, v49
	v_fma_f32 v52, -v48, v51, v50
	v_fmac_f32_e32 v51, v52, v49
	v_fma_f32 v48, -v48, v51, v50
	v_div_fmas_f32 v48, v48, v49, v51
	v_div_fixup_f32 v48, v48, s28, v47
	v_cmp_gt_f32_e64 vcc, s28, 0
	v_writelane_b32 v40, s28, 9
	s_nop 0
	v_cndmask_b32_e32 v48, 0, v48, vcc
	v_fmaak_f32 v49, v18, v48, 0x4b400000
	v_fmaak_f32 v50, v19, v48, 0x4b400000
	v_fmaak_f32 v51, v20, v48, 0x4b400000
	v_fmaak_f32 v52, v21, v48, 0x4b400000
	v_perm_b32 v49, v50, v49, s33
	v_perm_b32 v51, v52, v51, s34
	v_or_b32_e32 v92, v49, v51
	v_fmaak_f32 v41, v22, v48, 0x4b400000
	v_fmaak_f32 v42, v23, v48, 0x4b400000
	v_fmaak_f32 v43, v24, v48, 0x4b400000
	v_fmaak_f32 v44, v25, v48, 0x4b400000
	v_perm_b32 v41, v42, v41, s33
	v_perm_b32 v43, v44, v43, s34
	v_or_b32_e32 v93, v41, v43
	v_fmaak_f32 v49, v26, v48, 0x4b400000
	v_fmaak_f32 v50, v27, v48, 0x4b400000
	v_fmaak_f32 v51, v28, v48, 0x4b400000
	v_fmaak_f32 v52, v29, v48, 0x4b400000
	v_perm_b32 v49, v50, v49, s33
	v_perm_b32 v51, v52, v51, s34
	v_or_b32_e32 v94, v49, v51
	v_fmaak_f32 v41, v30, v48, 0x4b400000
	v_fmaak_f32 v42, v31, v48, 0x4b400000
	v_fmaak_f32 v43, v32, v48, 0x4b400000
	v_fmaak_f32 v44, v33, v48, 0x4b400000
	v_perm_b32 v41, v42, v41, s33
	v_perm_b32 v43, v44, v43, s34
	v_or_b32_e32 v95, v41, v43
	s_waitcnt vmcnt(0)
	ds_read_b128 v[18:21], v38 offset:0
	ds_read_b128 v[22:25], v38 offset:1024
	ds_read_b128 v[26:29], v38 offset:2048
	ds_read_b128 v[30:33], v38 offset:3072
	s_waitcnt lgkmcnt(0)
	s_barrier
	s_mov_b32 m0, s35
	s_nop 0
	global_load_lds_dwordx4 v34, s[16:17] nt
	global_load_lds_dwordx4 v34, s[16:17] offset:1024 nt
	global_load_lds_dwordx4 v34, s[16:17] offset:2048 nt
	global_load_lds_dwordx4 v35, s[16:17] offset:3072 nt
	s_add_u32 s16, s16, 0xfa0000
	s_addc_u32 s17, s17, 0
	v_cndmask_b32_e64 v30, 0, v30, s[18:19]
	v_cndmask_b32_e64 v31, 0, v31, s[18:19]
	v_cndmask_b32_e64 v32, 0, v32, s[18:19]
	v_cndmask_b32_e64 v33, 0, v33, s[18:19]
	v_max3_f32 v41, |v18|, |v19|, |v20|
	v_max3_f32 v42, |v21|, |v22|, |v23|
	v_max3_f32 v43, |v24|, |v25|, |v26|
	v_max3_f32 v44, |v27|, |v28|, |v29|
	v_max3_f32 v48, |v30|, |v31|, |v32|
	v_max3_f32 v41, v41, v42, |v33|
	v_max3_f32 v43, v43, v44, v48
	v_max_f32_e32 v41, v41, v43
	v_pk_add_f32 v[2:3], v[2:3], v[18:19]
	v_pk_add_f32 v[4:5], v[4:5], v[20:21]
	v_max_f32_dpp v41, v41, v41 quad_perm:[1,0,3,2] row_mask:0xf bank_mask:0xf
	v_pk_add_f32 v[6:7], v[6:7], v[22:23]
	v_pk_add_f32 v[8:9], v[8:9], v[24:25]
	v_max_f32_dpp v41, v41, v41 quad_perm:[2,3,0,1] row_mask:0xf bank_mask:0xf
	v_pk_add_f32 v[10:11], v[10:11], v[26:27]
	v_pk_add_f32 v[12:13], v[12:13], v[28:29]
	v_max_f32_dpp v41, v41, v41 row_half_mirror row_mask:0xf bank_mask:0xf
	v_pk_add_f32 v[14:15], v[14:15], v[30:31]
	v_pk_add_f32 v[16:17], v[16:17], v[32:33]
	v_max_f32_dpp v41, v41, v41 row_mirror row_mask:0xf bank_mask:0xf
	s_nop 1
	v_max_f32_dpp v41, v41, v41 row_bcast:15 row_mask:0xa bank_mask:0xf
	s_nop 1
	v_max_f32_dpp v41, v41, v41 row_bcast:31 row_mask:0xc bank_mask:0xf
	s_nop 1
	v_readlane_b32 s28, v41, 63
	s_nop 1
	v_div_scale_f32 v48, s[30:31], s28, s28, v47
	v_rcp_f32_e32 v49, v48
	s_nop 0
	v_fma_f32 v50, -v48, v49, 1.0
	v_fmac_f32_e32 v49, v50, v49
	v_mov_b32_e32 v50, s28
	v_div_scale_f32 v50, vcc, s32, v50, s32
	v_mul_f32_e32 v51, v50, v49
	v_fma_f32 v52, -v48, v51, v50
	v_fmac_f32_e32 v51, v52, v49
	v_fma_f32 v48, -v48, v51, v50
	v_div_fmas_f32 v48, v48, v49, v51
	v_div_fixup_f32 v48, v48, s28, v47
	v_cmp_gt_f32_e64 vcc, s28, 0
	v_writelane_b32 v40, s28, 10
	s_nop 0
	v_cndmask_b32_e32 v48, 0, v48, vcc
	v_fmaak_f32 v49, v18, v48, 0x4b400000
	v_fmaak_f32 v50, v19, v48, 0x4b400000
	v_fmaak_f32 v51, v20, v48, 0x4b400000
	v_fmaak_f32 v52, v21, v48, 0x4b400000
	v_perm_b32 v49, v50, v49, s33
	v_perm_b32 v51, v52, v51, s34
	v_or_b32_e32 v96, v49, v51
	v_fmaak_f32 v41, v22, v48, 0x4b400000
	v_fmaak_f32 v42, v23, v48, 0x4b400000
	v_fmaak_f32 v43, v24, v48, 0x4b400000
	v_fmaak_f32 v44, v25, v48, 0x4b400000
	v_perm_b32 v41, v42, v41, s33
	v_perm_b32 v43, v44, v43, s34
	v_or_b32_e32 v97, v41, v43
	v_fmaak_f32 v49, v26, v48, 0x4b400000
	v_fmaak_f32 v50, v27, v48, 0x4b400000
	v_fmaak_f32 v51, v28, v48, 0x4b400000
	v_fmaak_f32 v52, v29, v48, 0x4b400000
	v_perm_b32 v49, v50, v49, s33
	v_perm_b32 v51, v52, v51, s34
	v_or_b32_e32 v98, v49, v51
	v_fmaak_f32 v41, v30, v48, 0x4b400000
	v_fmaak_f32 v42, v31, v48, 0x4b400000
	v_fmaak_f32 v43, v32, v48, 0x4b400000
	v_fmaak_f32 v44, v33, v48, 0x4b400000
	v_perm_b32 v41, v42, v41, s33
	v_perm_b32 v43, v44, v43, s34
	v_or_b32_e32 v99, v41, v43
	s_waitcnt vmcnt(0)
	ds_read_b128 v[18:21], v38 offset:0
	ds_read_b128 v[22:25], v38 offset:1024
	ds_read_b128 v[26:29], v38 offset:2048
	ds_read_b128 v[30:33], v38 offset:3072
	s_waitcnt lgkmcnt(0)
	s_barrier
	s_mov_b32 m0, s35
	s_nop 0
	global_load_lds_dwordx4 v34, s[16:17] nt
	global_load_lds_dwordx4 v34, s[16:17] offset:1024 nt
	global_load_lds_dwordx4 v34, s[16:17] offset:2048 nt
	global_load_lds_dwordx4 v35, s[16:17] offset:3072 nt
	s_add_u32 s16, s16, 0xfa0000
	s_addc_u32 s17, s17, 0
	v_cndmask_b32_e64 v30, 0, v30, s[18:19]
	v_cndmask_b32_e64 v31, 0, v31, s[18:19]
	v_cndmask_b32_e64 v32, 0, v32, s[18:19]
	v_cndmask_b32_e64 v33, 0, v33, s[18:19]
	v_max3_f32 v41, |v18|, |v19|, |v20|
	v_max3_f32 v42, |v21|, |v22|, |v23|
	v_max3_f32 v43, |v24|, |v25|, |v26|
	v_max3_f32 v44, |v27|, |v28|, |v29|
	v_max3_f32 v48, |v30|, |v31|, |v32|
	v_max3_f32 v41, v41, v42, |v33|
	v_max3_f32 v43, v43, v44, v48
	v_max_f32_e32 v41, v41, v43
	v_pk_add_f32 v[2:3], v[2:3], v[18:19]
	v_pk_add_f32 v[4:5], v[4:5], v[20:21]
	v_max_f32_dpp v41, v41, v41 quad_perm:[1,0,3,2] row_mask:0xf bank_mask:0xf
	v_pk_add_f32 v[6:7], v[6:7], v[22:23]
	v_pk_add_f32 v[8:9], v[8:9], v[24:25]
	v_max_f32_dpp v41, v41, v41 quad_perm:[2,3,0,1] row_mask:0xf bank_mask:0xf
	v_pk_add_f32 v[10:11], v[10:11], v[26:27]
	v_pk_add_f32 v[12:13], v[12:13], v[28:29]
	v_max_f32_dpp v41, v41, v41 row_half_mirror row_mask:0xf bank_mask:0xf
	v_pk_add_f32 v[14:15], v[14:15], v[30:31]
	v_pk_add_f32 v[16:17], v[16:17], v[32:33]
	v_max_f32_dpp v41, v41, v41 row_mirror row_mask:0xf bank_mask:0xf
	s_nop 1
	v_max_f32_dpp v41, v41, v41 row_bcast:15 row_mask:0xa bank_mask:0xf
	s_nop 1
	v_max_f32_dpp v41, v41, v41 row_bcast:31 row_mask:0xc bank_mask:0xf
	s_nop 1
	v_readlane_b32 s28, v41, 63
	s_nop 1
	v_div_scale_f32 v48, s[30:31], s28, s28, v47
	v_rcp_f32_e32 v49, v48
	s_nop 0
	v_fma_f32 v50, -v48, v49, 1.0
	v_fmac_f32_e32 v49, v50, v49
	v_mov_b32_e32 v50, s28
	v_div_scale_f32 v50, vcc, s32, v50, s32
	v_mul_f32_e32 v51, v50, v49
	v_fma_f32 v52, -v48, v51, v50
	v_fmac_f32_e32 v51, v52, v49
	v_fma_f32 v48, -v48, v51, v50
	v_div_fmas_f32 v48, v48, v49, v51
	v_div_fixup_f32 v48, v48, s28, v47
	v_cmp_gt_f32_e64 vcc, s28, 0
	v_writelane_b32 v40, s28, 11
	s_nop 0
	v_cndmask_b32_e32 v48, 0, v48, vcc
	v_fmaak_f32 v49, v18, v48, 0x4b400000
	v_fmaak_f32 v50, v19, v48, 0x4b400000
	v_fmaak_f32 v51, v20, v48, 0x4b400000
	v_fmaak_f32 v52, v21, v48, 0x4b400000
	v_perm_b32 v49, v50, v49, s33
	v_perm_b32 v51, v52, v51, s34
	v_or_b32_e32 v100, v49, v51
	v_fmaak_f32 v41, v22, v48, 0x4b400000
	v_fmaak_f32 v42, v23, v48, 0x4b400000
	v_fmaak_f32 v43, v24, v48, 0x4b400000
	v_fmaak_f32 v44, v25, v48, 0x4b400000
	v_perm_b32 v41, v42, v41, s33
	v_perm_b32 v43, v44, v43, s34
	v_or_b32_e32 v101, v41, v43
	v_fmaak_f32 v49, v26, v48, 0x4b400000
	v_fmaak_f32 v50, v27, v48, 0x4b400000
	v_fmaak_f32 v51, v28, v48, 0x4b400000
	v_fmaak_f32 v52, v29, v48, 0x4b400000
	v_perm_b32 v49, v50, v49, s33
	v_perm_b32 v51, v52, v51, s34
	v_or_b32_e32 v102, v49, v51
	v_fmaak_f32 v41, v30, v48, 0x4b400000
	v_fmaak_f32 v42, v31, v48, 0x4b400000
	v_fmaak_f32 v43, v32, v48, 0x4b400000
	v_fmaak_f32 v44, v33, v48, 0x4b400000
	v_perm_b32 v41, v42, v41, s33
	v_perm_b32 v43, v44, v43, s34
	v_or_b32_e32 v103, v41, v43
	s_waitcnt vmcnt(0)
	ds_read_b128 v[18:21], v38 offset:0
	ds_read_b128 v[22:25], v38 offset:1024
	ds_read_b128 v[26:29], v38 offset:2048
	ds_read_b128 v[30:33], v38 offset:3072
	s_waitcnt lgkmcnt(0)
	s_barrier
	s_mov_b32 m0, s35
	s_nop 0
	global_load_lds_dwordx4 v34, s[16:17] nt
	global_load_lds_dwordx4 v34, s[16:17] offset:1024 nt
	global_load_lds_dwordx4 v34, s[16:17] offset:2048 nt
	global_load_lds_dwordx4 v35, s[16:17] offset:3072 nt
	s_add_u32 s16, s16, 0xfa0000
	s_addc_u32 s17, s17, 0
	v_cndmask_b32_e64 v30, 0, v30, s[18:19]
	v_cndmask_b32_e64 v31, 0, v31, s[18:19]
	v_cndmask_b32_e64 v32, 0, v32, s[18:19]
	v_cndmask_b32_e64 v33, 0, v33, s[18:19]
	v_max3_f32 v41, |v18|, |v19|, |v20|
	v_max3_f32 v42, |v21|, |v22|, |v23|
	v_max3_f32 v43, |v24|, |v25|, |v26|
	v_max3_f32 v44, |v27|, |v28|, |v29|
	v_max3_f32 v48, |v30|, |v31|, |v32|
	v_max3_f32 v41, v41, v42, |v33|
	v_max3_f32 v43, v43, v44, v48
	v_max_f32_e32 v41, v41, v43
	v_pk_add_f32 v[2:3], v[2:3], v[18:19]
	v_pk_add_f32 v[4:5], v[4:5], v[20:21]
	v_max_f32_dpp v41, v41, v41 quad_perm:[1,0,3,2] row_mask:0xf bank_mask:0xf
	v_pk_add_f32 v[6:7], v[6:7], v[22:23]
	v_pk_add_f32 v[8:9], v[8:9], v[24:25]
	v_max_f32_dpp v41, v41, v41 quad_perm:[2,3,0,1] row_mask:0xf bank_mask:0xf
	v_pk_add_f32 v[10:11], v[10:11], v[26:27]
	v_pk_add_f32 v[12:13], v[12:13], v[28:29]
	v_max_f32_dpp v41, v41, v41 row_half_mirror row_mask:0xf bank_mask:0xf
	v_pk_add_f32 v[14:15], v[14:15], v[30:31]
	v_pk_add_f32 v[16:17], v[16:17], v[32:33]
	v_max_f32_dpp v41, v41, v41 row_mirror row_mask:0xf bank_mask:0xf
	s_nop 1
	v_max_f32_dpp v41, v41, v41 row_bcast:15 row_mask:0xa bank_mask:0xf
	s_nop 1
	v_max_f32_dpp v41, v41, v41 row_bcast:31 row_mask:0xc bank_mask:0xf
	s_nop 1
	v_readlane_b32 s28, v41, 63
	s_nop 1
	v_div_scale_f32 v48, s[30:31], s28, s28, v47
	v_rcp_f32_e32 v49, v48
	s_nop 0
	v_fma_f32 v50, -v48, v49, 1.0
	v_fmac_f32_e32 v49, v50, v49
	v_mov_b32_e32 v50, s28
	v_div_scale_f32 v50, vcc, s32, v50, s32
	v_mul_f32_e32 v51, v50, v49
	v_fma_f32 v52, -v48, v51, v50
	v_fmac_f32_e32 v51, v52, v49
	v_fma_f32 v48, -v48, v51, v50
	v_div_fmas_f32 v48, v48, v49, v51
	v_div_fixup_f32 v48, v48, s28, v47
	v_cmp_gt_f32_e64 vcc, s28, 0
	v_writelane_b32 v40, s28, 12
	s_nop 0
	v_cndmask_b32_e32 v48, 0, v48, vcc
	v_fmaak_f32 v49, v18, v48, 0x4b400000
	v_fmaak_f32 v50, v19, v48, 0x4b400000
	v_fmaak_f32 v51, v20, v48, 0x4b400000
	v_fmaak_f32 v52, v21, v48, 0x4b400000
	v_perm_b32 v49, v50, v49, s33
	v_perm_b32 v51, v52, v51, s34
	v_or_b32_e32 v104, v49, v51
	v_fmaak_f32 v41, v22, v48, 0x4b400000
	v_fmaak_f32 v42, v23, v48, 0x4b400000
	v_fmaak_f32 v43, v24, v48, 0x4b400000
	v_fmaak_f32 v44, v25, v48, 0x4b400000
	v_perm_b32 v41, v42, v41, s33
	v_perm_b32 v43, v44, v43, s34
	v_or_b32_e32 v105, v41, v43
	v_fmaak_f32 v49, v26, v48, 0x4b400000
	v_fmaak_f32 v50, v27, v48, 0x4b400000
	v_fmaak_f32 v51, v28, v48, 0x4b400000
	v_fmaak_f32 v52, v29, v48, 0x4b400000
	v_perm_b32 v49, v50, v49, s33
	v_perm_b32 v51, v52, v51, s34
	v_or_b32_e32 v106, v49, v51
	v_fmaak_f32 v41, v30, v48, 0x4b400000
	v_fmaak_f32 v42, v31, v48, 0x4b400000
	v_fmaak_f32 v43, v32, v48, 0x4b400000
	v_fmaak_f32 v44, v33, v48, 0x4b400000
	v_perm_b32 v41, v42, v41, s33
	v_perm_b32 v43, v44, v43, s34
	v_or_b32_e32 v107, v41, v43
	s_waitcnt vmcnt(0)
	ds_read_b128 v[18:21], v38 offset:0
	ds_read_b128 v[22:25], v38 offset:1024
	ds_read_b128 v[26:29], v38 offset:2048
	ds_read_b128 v[30:33], v38 offset:3072
	s_waitcnt lgkmcnt(0)
	s_barrier
	s_mov_b32 m0, s35
	s_nop 0
	global_load_lds_dwordx4 v34, s[16:17] nt
	global_load_lds_dwordx4 v34, s[16:17] offset:1024 nt
	global_load_lds_dwordx4 v34, s[16:17] offset:2048 nt
	global_load_lds_dwordx4 v35, s[16:17] offset:3072 nt
	s_add_u32 s16, s16, 0xfa0000
	s_addc_u32 s17, s17, 0
	v_cndmask_b32_e64 v30, 0, v30, s[18:19]
	v_cndmask_b32_e64 v31, 0, v31, s[18:19]
	v_cndmask_b32_e64 v32, 0, v32, s[18:19]
	v_cndmask_b32_e64 v33, 0, v33, s[18:19]
	v_max3_f32 v41, |v18|, |v19|, |v20|
	v_max3_f32 v42, |v21|, |v22|, |v23|
	v_max3_f32 v43, |v24|, |v25|, |v26|
	v_max3_f32 v44, |v27|, |v28|, |v29|
	v_max3_f32 v48, |v30|, |v31|, |v32|
	v_max3_f32 v41, v41, v42, |v33|
	v_max3_f32 v43, v43, v44, v48
	v_max_f32_e32 v41, v41, v43
	v_pk_add_f32 v[2:3], v[2:3], v[18:19]
	v_pk_add_f32 v[4:5], v[4:5], v[20:21]
	v_max_f32_dpp v41, v41, v41 quad_perm:[1,0,3,2] row_mask:0xf bank_mask:0xf
	v_pk_add_f32 v[6:7], v[6:7], v[22:23]
	v_pk_add_f32 v[8:9], v[8:9], v[24:25]
	v_max_f32_dpp v41, v41, v41 quad_perm:[2,3,0,1] row_mask:0xf bank_mask:0xf
	v_pk_add_f32 v[10:11], v[10:11], v[26:27]
	v_pk_add_f32 v[12:13], v[12:13], v[28:29]
	v_max_f32_dpp v41, v41, v41 row_half_mirror row_mask:0xf bank_mask:0xf
	v_pk_add_f32 v[14:15], v[14:15], v[30:31]
	v_pk_add_f32 v[16:17], v[16:17], v[32:33]
	v_max_f32_dpp v41, v41, v41 row_mirror row_mask:0xf bank_mask:0xf
	s_nop 1
	v_max_f32_dpp v41, v41, v41 row_bcast:15 row_mask:0xa bank_mask:0xf
	s_nop 1
	v_max_f32_dpp v41, v41, v41 row_bcast:31 row_mask:0xc bank_mask:0xf
	s_nop 1
	v_readlane_b32 s28, v41, 63
	s_nop 1
	v_div_scale_f32 v48, s[30:31], s28, s28, v47
	v_rcp_f32_e32 v49, v48
	s_nop 0
	v_fma_f32 v50, -v48, v49, 1.0
	v_fmac_f32_e32 v49, v50, v49
	v_mov_b32_e32 v50, s28
	v_div_scale_f32 v50, vcc, s32, v50, s32
	v_mul_f32_e32 v51, v50, v49
	v_fma_f32 v52, -v48, v51, v50
	v_fmac_f32_e32 v51, v52, v49
	v_fma_f32 v48, -v48, v51, v50
	v_div_fmas_f32 v48, v48, v49, v51
	v_div_fixup_f32 v48, v48, s28, v47
	v_cmp_gt_f32_e64 vcc, s28, 0
	v_writelane_b32 v40, s28, 13
	s_nop 0
	v_cndmask_b32_e32 v48, 0, v48, vcc
	v_fmaak_f32 v49, v18, v48, 0x4b400000
	v_fmaak_f32 v50, v19, v48, 0x4b400000
	v_fmaak_f32 v51, v20, v48, 0x4b400000
	v_fmaak_f32 v52, v21, v48, 0x4b400000
	v_perm_b32 v49, v50, v49, s33
	v_perm_b32 v51, v52, v51, s34
	v_or_b32_e32 v108, v49, v51
	v_fmaak_f32 v41, v22, v48, 0x4b400000
	v_fmaak_f32 v42, v23, v48, 0x4b400000
	v_fmaak_f32 v43, v24, v48, 0x4b400000
	v_fmaak_f32 v44, v25, v48, 0x4b400000
	v_perm_b32 v41, v42, v41, s33
	v_perm_b32 v43, v44, v43, s34
	v_or_b32_e32 v109, v41, v43
	v_fmaak_f32 v49, v26, v48, 0x4b400000
	v_fmaak_f32 v50, v27, v48, 0x4b400000
	v_fmaak_f32 v51, v28, v48, 0x4b400000
	v_fmaak_f32 v52, v29, v48, 0x4b400000
	v_perm_b32 v49, v50, v49, s33
	v_perm_b32 v51, v52, v51, s34
	v_or_b32_e32 v110, v49, v51
	v_fmaak_f32 v41, v30, v48, 0x4b400000
	v_fmaak_f32 v42, v31, v48, 0x4b400000
	v_fmaak_f32 v43, v32, v48, 0x4b400000
	v_fmaak_f32 v44, v33, v48, 0x4b400000
	v_perm_b32 v41, v42, v41, s33
	v_perm_b32 v43, v44, v43, s34
	v_or_b32_e32 v111, v41, v43
	s_waitcnt vmcnt(0)
	ds_read_b128 v[18:21], v38 offset:0
	ds_read_b128 v[22:25], v38 offset:1024
	ds_read_b128 v[26:29], v38 offset:2048
	ds_read_b128 v[30:33], v38 offset:3072
	s_waitcnt lgkmcnt(0)
	s_barrier
	s_mov_b32 m0, s35
	s_nop 0
	global_load_lds_dwordx4 v34, s[16:17] nt
	global_load_lds_dwordx4 v34, s[16:17] offset:1024 nt
	global_load_lds_dwordx4 v34, s[16:17] offset:2048 nt
	global_load_lds_dwordx4 v35, s[16:17] offset:3072 nt
	s_add_u32 s16, s16, 0xfa0000
	s_addc_u32 s17, s17, 0
	v_cndmask_b32_e64 v30, 0, v30, s[18:19]
	v_cndmask_b32_e64 v31, 0, v31, s[18:19]
	v_cndmask_b32_e64 v32, 0, v32, s[18:19]
	v_cndmask_b32_e64 v33, 0, v33, s[18:19]
	v_max3_f32 v41, |v18|, |v19|, |v20|
	v_max3_f32 v42, |v21|, |v22|, |v23|
	v_max3_f32 v43, |v24|, |v25|, |v26|
	v_max3_f32 v44, |v27|, |v28|, |v29|
	v_max3_f32 v48, |v30|, |v31|, |v32|
	v_max3_f32 v41, v41, v42, |v33|
	v_max3_f32 v43, v43, v44, v48
	v_max_f32_e32 v41, v41, v43
	v_pk_add_f32 v[2:3], v[2:3], v[18:19]
	v_pk_add_f32 v[4:5], v[4:5], v[20:21]
	v_max_f32_dpp v41, v41, v41 quad_perm:[1,0,3,2] row_mask:0xf bank_mask:0xf
	v_pk_add_f32 v[6:7], v[6:7], v[22:23]
	v_pk_add_f32 v[8:9], v[8:9], v[24:25]
	v_max_f32_dpp v41, v41, v41 quad_perm:[2,3,0,1] row_mask:0xf bank_mask:0xf
	v_pk_add_f32 v[10:11], v[10:11], v[26:27]
	v_pk_add_f32 v[12:13], v[12:13], v[28:29]
	v_max_f32_dpp v41, v41, v41 row_half_mirror row_mask:0xf bank_mask:0xf
	v_pk_add_f32 v[14:15], v[14:15], v[30:31]
	v_pk_add_f32 v[16:17], v[16:17], v[32:33]
	v_max_f32_dpp v41, v41, v41 row_mirror row_mask:0xf bank_mask:0xf
	s_nop 1
	v_max_f32_dpp v41, v41, v41 row_bcast:15 row_mask:0xa bank_mask:0xf
	s_nop 1
	v_max_f32_dpp v41, v41, v41 row_bcast:31 row_mask:0xc bank_mask:0xf
	s_nop 1
	v_readlane_b32 s28, v41, 63
	s_nop 1
	v_div_scale_f32 v48, s[30:31], s28, s28, v47
	v_rcp_f32_e32 v49, v48
	s_nop 0
	v_fma_f32 v50, -v48, v49, 1.0
	v_fmac_f32_e32 v49, v50, v49
	v_mov_b32_e32 v50, s28
	v_div_scale_f32 v50, vcc, s32, v50, s32
	v_mul_f32_e32 v51, v50, v49
	v_fma_f32 v52, -v48, v51, v50
	v_fmac_f32_e32 v51, v52, v49
	v_fma_f32 v48, -v48, v51, v50
	v_div_fmas_f32 v48, v48, v49, v51
	v_div_fixup_f32 v48, v48, s28, v47
	v_cmp_gt_f32_e64 vcc, s28, 0
	v_writelane_b32 v40, s28, 14
	s_nop 0
	v_cndmask_b32_e32 v48, 0, v48, vcc
	v_fmaak_f32 v49, v18, v48, 0x4b400000
	v_fmaak_f32 v50, v19, v48, 0x4b400000
	v_fmaak_f32 v51, v20, v48, 0x4b400000
	v_fmaak_f32 v52, v21, v48, 0x4b400000
	v_perm_b32 v49, v50, v49, s33
	v_perm_b32 v51, v52, v51, s34
	v_or_b32_e32 v112, v49, v51
	v_fmaak_f32 v41, v22, v48, 0x4b400000
	v_fmaak_f32 v42, v23, v48, 0x4b400000
	v_fmaak_f32 v43, v24, v48, 0x4b400000
	v_fmaak_f32 v44, v25, v48, 0x4b400000
	v_perm_b32 v41, v42, v41, s33
	v_perm_b32 v43, v44, v43, s34
	v_or_b32_e32 v113, v41, v43
	v_fmaak_f32 v49, v26, v48, 0x4b400000
	v_fmaak_f32 v50, v27, v48, 0x4b400000
	v_fmaak_f32 v51, v28, v48, 0x4b400000
	v_fmaak_f32 v52, v29, v48, 0x4b400000
	v_perm_b32 v49, v50, v49, s33
	v_perm_b32 v51, v52, v51, s34
	v_or_b32_e32 v114, v49, v51
	v_fmaak_f32 v41, v30, v48, 0x4b400000
	v_fmaak_f32 v42, v31, v48, 0x4b400000
	v_fmaak_f32 v43, v32, v48, 0x4b400000
	v_fmaak_f32 v44, v33, v48, 0x4b400000
	v_perm_b32 v41, v42, v41, s33
	v_perm_b32 v43, v44, v43, s34
	v_or_b32_e32 v115, v41, v43
	s_waitcnt vmcnt(0)
	ds_read_b128 v[18:21], v38 offset:0
	ds_read_b128 v[22:25], v38 offset:1024
	ds_read_b128 v[26:29], v38 offset:2048
	ds_read_b128 v[30:33], v38 offset:3072
	s_waitcnt lgkmcnt(0)
	s_barrier
	s_mov_b32 m0, s35
	s_nop 0
	global_load_lds_dwordx4 v34, s[16:17] nt
	global_load_lds_dwordx4 v34, s[16:17] offset:1024 nt
	global_load_lds_dwordx4 v34, s[16:17] offset:2048 nt
	global_load_lds_dwordx4 v35, s[16:17] offset:3072 nt
	s_add_u32 s16, s16, 0xfa0000
	s_addc_u32 s17, s17, 0
	v_cndmask_b32_e64 v30, 0, v30, s[18:19]
	v_cndmask_b32_e64 v31, 0, v31, s[18:19]
	v_cndmask_b32_e64 v32, 0, v32, s[18:19]
	v_cndmask_b32_e64 v33, 0, v33, s[18:19]
	v_max3_f32 v41, |v18|, |v19|, |v20|
	v_max3_f32 v42, |v21|, |v22|, |v23|
	v_max3_f32 v43, |v24|, |v25|, |v26|
	v_max3_f32 v44, |v27|, |v28|, |v29|
	v_max3_f32 v48, |v30|, |v31|, |v32|
	v_max3_f32 v41, v41, v42, |v33|
	v_max3_f32 v43, v43, v44, v48
	v_max_f32_e32 v41, v41, v43
	v_pk_add_f32 v[2:3], v[2:3], v[18:19]
	v_pk_add_f32 v[4:5], v[4:5], v[20:21]
	v_max_f32_dpp v41, v41, v41 quad_perm:[1,0,3,2] row_mask:0xf bank_mask:0xf
	v_pk_add_f32 v[6:7], v[6:7], v[22:23]
	v_pk_add_f32 v[8:9], v[8:9], v[24:25]
	v_max_f32_dpp v41, v41, v41 quad_perm:[2,3,0,1] row_mask:0xf bank_mask:0xf
	v_pk_add_f32 v[10:11], v[10:11], v[26:27]
	v_pk_add_f32 v[12:13], v[12:13], v[28:29]
	v_max_f32_dpp v41, v41, v41 row_half_mirror row_mask:0xf bank_mask:0xf
	v_pk_add_f32 v[14:15], v[14:15], v[30:31]
	v_pk_add_f32 v[16:17], v[16:17], v[32:33]
	v_max_f32_dpp v41, v41, v41 row_mirror row_mask:0xf bank_mask:0xf
	s_nop 1
	v_max_f32_dpp v41, v41, v41 row_bcast:15 row_mask:0xa bank_mask:0xf
	s_nop 1
	v_max_f32_dpp v41, v41, v41 row_bcast:31 row_mask:0xc bank_mask:0xf
	s_nop 1
	v_readlane_b32 s28, v41, 63
	s_nop 1
	v_div_scale_f32 v48, s[30:31], s28, s28, v47
	v_rcp_f32_e32 v49, v48
	s_nop 0
	v_fma_f32 v50, -v48, v49, 1.0
	v_fmac_f32_e32 v49, v50, v49
	v_mov_b32_e32 v50, s28
	v_div_scale_f32 v50, vcc, s32, v50, s32
	v_mul_f32_e32 v51, v50, v49
	v_fma_f32 v52, -v48, v51, v50
	v_fmac_f32_e32 v51, v52, v49
	v_fma_f32 v48, -v48, v51, v50
	v_div_fmas_f32 v48, v48, v49, v51
	v_div_fixup_f32 v48, v48, s28, v47
	v_cmp_gt_f32_e64 vcc, s28, 0
	v_writelane_b32 v40, s28, 15
	s_nop 0
	v_cndmask_b32_e32 v48, 0, v48, vcc
	v_fmaak_f32 v49, v18, v48, 0x4b400000
	v_fmaak_f32 v50, v19, v48, 0x4b400000
	v_fmaak_f32 v51, v20, v48, 0x4b400000
	v_fmaak_f32 v52, v21, v48, 0x4b400000
	v_perm_b32 v49, v50, v49, s33
	v_perm_b32 v51, v52, v51, s34
	v_or_b32_e32 v116, v49, v51
	v_fmaak_f32 v41, v22, v48, 0x4b400000
	v_fmaak_f32 v42, v23, v48, 0x4b400000
	v_fmaak_f32 v43, v24, v48, 0x4b400000
	v_fmaak_f32 v44, v25, v48, 0x4b400000
	v_perm_b32 v41, v42, v41, s33
	v_perm_b32 v43, v44, v43, s34
	v_or_b32_e32 v117, v41, v43
	v_fmaak_f32 v49, v26, v48, 0x4b400000
	v_fmaak_f32 v50, v27, v48, 0x4b400000
	v_fmaak_f32 v51, v28, v48, 0x4b400000
	v_fmaak_f32 v52, v29, v48, 0x4b400000
	v_perm_b32 v49, v50, v49, s33
	v_perm_b32 v51, v52, v51, s34
	v_or_b32_e32 v118, v49, v51
	v_fmaak_f32 v41, v30, v48, 0x4b400000
	v_fmaak_f32 v42, v31, v48, 0x4b400000
	v_fmaak_f32 v43, v32, v48, 0x4b400000
	v_fmaak_f32 v44, v33, v48, 0x4b400000
	v_perm_b32 v41, v42, v41, s33
	v_perm_b32 v43, v44, v43, s34
	v_or_b32_e32 v119, v41, v43
	s_waitcnt vmcnt(0)
	ds_read_b128 v[18:21], v38 offset:0
	ds_read_b128 v[22:25], v38 offset:1024
	ds_read_b128 v[26:29], v38 offset:2048
	ds_read_b128 v[30:33], v38 offset:3072
	s_waitcnt lgkmcnt(0)
	s_barrier
	s_mov_b32 m0, s35
	s_nop 0
	global_load_lds_dwordx4 v34, s[16:17] nt
	global_load_lds_dwordx4 v34, s[16:17] offset:1024 nt
	global_load_lds_dwordx4 v34, s[16:17] offset:2048 nt
	global_load_lds_dwordx4 v35, s[16:17] offset:3072 nt
	s_add_u32 s16, s16, 0xfa0000
	s_addc_u32 s17, s17, 0
	v_cndmask_b32_e64 v30, 0, v30, s[18:19]
	v_cndmask_b32_e64 v31, 0, v31, s[18:19]
	v_cndmask_b32_e64 v32, 0, v32, s[18:19]
	v_cndmask_b32_e64 v33, 0, v33, s[18:19]
	v_max3_f32 v41, |v18|, |v19|, |v20|
	v_max3_f32 v42, |v21|, |v22|, |v23|
	v_max3_f32 v43, |v24|, |v25|, |v26|
	v_max3_f32 v44, |v27|, |v28|, |v29|
	v_max3_f32 v48, |v30|, |v31|, |v32|
	v_max3_f32 v41, v41, v42, |v33|
	v_max3_f32 v43, v43, v44, v48
	v_max_f32_e32 v41, v41, v43
	v_pk_add_f32 v[2:3], v[2:3], v[18:19]
	v_pk_add_f32 v[4:5], v[4:5], v[20:21]
	v_max_f32_dpp v41, v41, v41 quad_perm:[1,0,3,2] row_mask:0xf bank_mask:0xf
	v_pk_add_f32 v[6:7], v[6:7], v[22:23]
	v_pk_add_f32 v[8:9], v[8:9], v[24:25]
	v_max_f32_dpp v41, v41, v41 quad_perm:[2,3,0,1] row_mask:0xf bank_mask:0xf
	v_pk_add_f32 v[10:11], v[10:11], v[26:27]
	v_pk_add_f32 v[12:13], v[12:13], v[28:29]
	v_max_f32_dpp v41, v41, v41 row_half_mirror row_mask:0xf bank_mask:0xf
	v_pk_add_f32 v[14:15], v[14:15], v[30:31]
	v_pk_add_f32 v[16:17], v[16:17], v[32:33]
	v_max_f32_dpp v41, v41, v41 row_mirror row_mask:0xf bank_mask:0xf
	s_nop 1
	v_max_f32_dpp v41, v41, v41 row_bcast:15 row_mask:0xa bank_mask:0xf
	s_nop 1
	v_max_f32_dpp v41, v41, v41 row_bcast:31 row_mask:0xc bank_mask:0xf
	s_nop 1
	v_readlane_b32 s28, v41, 63
	s_nop 1
	v_div_scale_f32 v48, s[30:31], s28, s28, v47
	v_rcp_f32_e32 v49, v48
	s_nop 0
	v_fma_f32 v50, -v48, v49, 1.0
	v_fmac_f32_e32 v49, v50, v49
	v_mov_b32_e32 v50, s28
	v_div_scale_f32 v50, vcc, s32, v50, s32
	v_mul_f32_e32 v51, v50, v49
	v_fma_f32 v52, -v48, v51, v50
	v_fmac_f32_e32 v51, v52, v49
	v_fma_f32 v48, -v48, v51, v50
	v_div_fmas_f32 v48, v48, v49, v51
	v_div_fixup_f32 v48, v48, s28, v47
	v_cmp_gt_f32_e64 vcc, s28, 0
	v_writelane_b32 v40, s28, 16
	s_nop 0
	v_cndmask_b32_e32 v48, 0, v48, vcc
	v_fmaak_f32 v49, v18, v48, 0x4b400000
	v_fmaak_f32 v50, v19, v48, 0x4b400000
	v_fmaak_f32 v51, v20, v48, 0x4b400000
	v_fmaak_f32 v52, v21, v48, 0x4b400000
	v_perm_b32 v49, v50, v49, s33
	v_perm_b32 v51, v52, v51, s34
	v_or_b32_e32 v120, v49, v51
	v_fmaak_f32 v41, v22, v48, 0x4b400000
	v_fmaak_f32 v42, v23, v48, 0x4b400000
	v_fmaak_f32 v43, v24, v48, 0x4b400000
	v_fmaak_f32 v44, v25, v48, 0x4b400000
	v_perm_b32 v41, v42, v41, s33
	v_perm_b32 v43, v44, v43, s34
	v_or_b32_e32 v121, v41, v43
	v_fmaak_f32 v49, v26, v48, 0x4b400000
	v_fmaak_f32 v50, v27, v48, 0x4b400000
	v_fmaak_f32 v51, v28, v48, 0x4b400000
	v_fmaak_f32 v52, v29, v48, 0x4b400000
	v_perm_b32 v49, v50, v49, s33
	v_perm_b32 v51, v52, v51, s34
	v_or_b32_e32 v122, v49, v51
	v_fmaak_f32 v41, v30, v48, 0x4b400000
	v_fmaak_f32 v42, v31, v48, 0x4b400000
	v_fmaak_f32 v43, v32, v48, 0x4b400000
	v_fmaak_f32 v44, v33, v48, 0x4b400000
	v_perm_b32 v41, v42, v41, s33
	v_perm_b32 v43, v44, v43, s34
	v_or_b32_e32 v123, v41, v43
	s_waitcnt vmcnt(0)
	ds_read_b128 v[18:21], v38 offset:0
	ds_read_b128 v[22:25], v38 offset:1024
	ds_read_b128 v[26:29], v38 offset:2048
	ds_read_b128 v[30:33], v38 offset:3072
	s_waitcnt lgkmcnt(0)
	s_barrier
	s_mov_b32 m0, s35
	s_nop 0
	global_load_lds_dwordx4 v34, s[16:17] nt
	global_load_lds_dwordx4 v34, s[16:17] offset:1024 nt
	global_load_lds_dwordx4 v34, s[16:17] offset:2048 nt
	global_load_lds_dwordx4 v35, s[16:17] offset:3072 nt
	s_add_u32 s16, s16, 0xfa0000
	s_addc_u32 s17, s17, 0
	v_cndmask_b32_e64 v30, 0, v30, s[18:19]
	v_cndmask_b32_e64 v31, 0, v31, s[18:19]
	v_cndmask_b32_e64 v32, 0, v32, s[18:19]
	v_cndmask_b32_e64 v33, 0, v33, s[18:19]
	v_max3_f32 v41, |v18|, |v19|, |v20|
	v_max3_f32 v42, |v21|, |v22|, |v23|
	v_max3_f32 v43, |v24|, |v25|, |v26|
	v_max3_f32 v44, |v27|, |v28|, |v29|
	v_max3_f32 v48, |v30|, |v31|, |v32|
	v_max3_f32 v41, v41, v42, |v33|
	v_max3_f32 v43, v43, v44, v48
	v_max_f32_e32 v41, v41, v43
	v_pk_add_f32 v[2:3], v[2:3], v[18:19]
	v_pk_add_f32 v[4:5], v[4:5], v[20:21]
	v_max_f32_dpp v41, v41, v41 quad_perm:[1,0,3,2] row_mask:0xf bank_mask:0xf
	v_pk_add_f32 v[6:7], v[6:7], v[22:23]
	v_pk_add_f32 v[8:9], v[8:9], v[24:25]
	v_max_f32_dpp v41, v41, v41 quad_perm:[2,3,0,1] row_mask:0xf bank_mask:0xf
	v_pk_add_f32 v[10:11], v[10:11], v[26:27]
	v_pk_add_f32 v[12:13], v[12:13], v[28:29]
	v_max_f32_dpp v41, v41, v41 row_half_mirror row_mask:0xf bank_mask:0xf
	v_pk_add_f32 v[14:15], v[14:15], v[30:31]
	v_pk_add_f32 v[16:17], v[16:17], v[32:33]
	v_max_f32_dpp v41, v41, v41 row_mirror row_mask:0xf bank_mask:0xf
	s_nop 1
	v_max_f32_dpp v41, v41, v41 row_bcast:15 row_mask:0xa bank_mask:0xf
	s_nop 1
	v_max_f32_dpp v41, v41, v41 row_bcast:31 row_mask:0xc bank_mask:0xf
	s_nop 1
	v_readlane_b32 s28, v41, 63
	s_nop 1
	v_div_scale_f32 v48, s[30:31], s28, s28, v47
	v_rcp_f32_e32 v49, v48
	s_nop 0
	v_fma_f32 v50, -v48, v49, 1.0
	v_fmac_f32_e32 v49, v50, v49
	v_mov_b32_e32 v50, s28
	v_div_scale_f32 v50, vcc, s32, v50, s32
	v_mul_f32_e32 v51, v50, v49
	v_fma_f32 v52, -v48, v51, v50
	v_fmac_f32_e32 v51, v52, v49
	v_fma_f32 v48, -v48, v51, v50
	v_div_fmas_f32 v48, v48, v49, v51
	v_div_fixup_f32 v48, v48, s28, v47
	v_cmp_gt_f32_e64 vcc, s28, 0
	v_writelane_b32 v40, s28, 17
	s_nop 0
	v_cndmask_b32_e32 v48, 0, v48, vcc
	v_fmaak_f32 v49, v18, v48, 0x4b400000
	v_fmaak_f32 v50, v19, v48, 0x4b400000
	v_fmaak_f32 v51, v20, v48, 0x4b400000
	v_fmaak_f32 v52, v21, v48, 0x4b400000
	v_perm_b32 v49, v50, v49, s33
	v_perm_b32 v51, v52, v51, s34
	v_or_b32_e32 v124, v49, v51
	v_fmaak_f32 v41, v22, v48, 0x4b400000
	v_fmaak_f32 v42, v23, v48, 0x4b400000
	v_fmaak_f32 v43, v24, v48, 0x4b400000
	v_fmaak_f32 v44, v25, v48, 0x4b400000
	v_perm_b32 v41, v42, v41, s33
	v_perm_b32 v43, v44, v43, s34
	v_or_b32_e32 v125, v41, v43
	v_fmaak_f32 v49, v26, v48, 0x4b400000
	v_fmaak_f32 v50, v27, v48, 0x4b400000
	v_fmaak_f32 v51, v28, v48, 0x4b400000
	v_fmaak_f32 v52, v29, v48, 0x4b400000
	v_perm_b32 v49, v50, v49, s33
	v_perm_b32 v51, v52, v51, s34
	v_or_b32_e32 v126, v49, v51
	v_fmaak_f32 v41, v30, v48, 0x4b400000
	v_fmaak_f32 v42, v31, v48, 0x4b400000
	v_fmaak_f32 v43, v32, v48, 0x4b400000
	v_fmaak_f32 v44, v33, v48, 0x4b400000
	v_perm_b32 v41, v42, v41, s33
	v_perm_b32 v43, v44, v43, s34
	v_or_b32_e32 v127, v41, v43
	s_waitcnt vmcnt(0)
	ds_read_b128 v[18:21], v38 offset:0
	ds_read_b128 v[22:25], v38 offset:1024
	ds_read_b128 v[26:29], v38 offset:2048
	ds_read_b128 v[30:33], v38 offset:3072
	s_waitcnt lgkmcnt(0)
	s_barrier
	s_mov_b32 m0, s35
	s_nop 0
	global_load_lds_dwordx4 v34, s[16:17] nt
	global_load_lds_dwordx4 v34, s[16:17] offset:1024 nt
	global_load_lds_dwordx4 v34, s[16:17] offset:2048 nt
	global_load_lds_dwordx4 v35, s[16:17] offset:3072 nt
	s_add_u32 s16, s16, 0xfa0000
	s_addc_u32 s17, s17, 0
	v_cndmask_b32_e64 v30, 0, v30, s[18:19]
	v_cndmask_b32_e64 v31, 0, v31, s[18:19]
	v_cndmask_b32_e64 v32, 0, v32, s[18:19]
	v_cndmask_b32_e64 v33, 0, v33, s[18:19]
	v_max3_f32 v41, |v18|, |v19|, |v20|
	v_max3_f32 v42, |v21|, |v22|, |v23|
	v_max3_f32 v43, |v24|, |v25|, |v26|
	v_max3_f32 v44, |v27|, |v28|, |v29|
	v_max3_f32 v48, |v30|, |v31|, |v32|
	v_max3_f32 v41, v41, v42, |v33|
	v_max3_f32 v43, v43, v44, v48
	v_max_f32_e32 v41, v41, v43
	v_pk_add_f32 v[2:3], v[2:3], v[18:19]
	v_pk_add_f32 v[4:5], v[4:5], v[20:21]
	v_max_f32_dpp v41, v41, v41 quad_perm:[1,0,3,2] row_mask:0xf bank_mask:0xf
	v_pk_add_f32 v[6:7], v[6:7], v[22:23]
	v_pk_add_f32 v[8:9], v[8:9], v[24:25]
	v_max_f32_dpp v41, v41, v41 quad_perm:[2,3,0,1] row_mask:0xf bank_mask:0xf
	v_pk_add_f32 v[10:11], v[10:11], v[26:27]
	v_pk_add_f32 v[12:13], v[12:13], v[28:29]
	v_max_f32_dpp v41, v41, v41 row_half_mirror row_mask:0xf bank_mask:0xf
	v_pk_add_f32 v[14:15], v[14:15], v[30:31]
	v_pk_add_f32 v[16:17], v[16:17], v[32:33]
	v_max_f32_dpp v41, v41, v41 row_mirror row_mask:0xf bank_mask:0xf
	s_nop 1
	v_max_f32_dpp v41, v41, v41 row_bcast:15 row_mask:0xa bank_mask:0xf
	s_nop 1
	v_max_f32_dpp v41, v41, v41 row_bcast:31 row_mask:0xc bank_mask:0xf
	s_nop 1
	v_readlane_b32 s28, v41, 63
	s_nop 1
	v_div_scale_f32 v48, s[30:31], s28, s28, v47
	v_rcp_f32_e32 v49, v48
	s_nop 0
	v_fma_f32 v50, -v48, v49, 1.0
	v_fmac_f32_e32 v49, v50, v49
	v_mov_b32_e32 v50, s28
	v_div_scale_f32 v50, vcc, s32, v50, s32
	v_mul_f32_e32 v51, v50, v49
	v_fma_f32 v52, -v48, v51, v50
	v_fmac_f32_e32 v51, v52, v49
	v_fma_f32 v48, -v48, v51, v50
	v_div_fmas_f32 v48, v48, v49, v51
	v_div_fixup_f32 v48, v48, s28, v47
	v_cmp_gt_f32_e64 vcc, s28, 0
	v_writelane_b32 v40, s28, 18
	s_nop 0
	v_cndmask_b32_e32 v48, 0, v48, vcc
	v_fmaak_f32 v49, v18, v48, 0x4b400000
	v_fmaak_f32 v50, v19, v48, 0x4b400000
	v_fmaak_f32 v51, v20, v48, 0x4b400000
	v_fmaak_f32 v52, v21, v48, 0x4b400000
	v_perm_b32 v49, v50, v49, s33
	v_perm_b32 v51, v52, v51, s34
	v_or_b32_e32 v36, v49, v51
	v_fmaak_f32 v41, v22, v48, 0x4b400000
	v_fmaak_f32 v42, v23, v48, 0x4b400000
	v_fmaak_f32 v43, v24, v48, 0x4b400000
	v_fmaak_f32 v44, v25, v48, 0x4b400000
	v_perm_b32 v41, v42, v41, s33
	v_perm_b32 v43, v44, v43, s34
	v_or_b32_e32 v37, v41, v43
	v_fmaak_f32 v49, v26, v48, 0x4b400000
	v_fmaak_f32 v50, v27, v48, 0x4b400000
	v_fmaak_f32 v51, v28, v48, 0x4b400000
	v_fmaak_f32 v52, v29, v48, 0x4b400000
	v_perm_b32 v49, v50, v49, s33
	v_perm_b32 v51, v52, v51, s34
	v_or_b32_e32 v45, v49, v51
	v_fmaak_f32 v41, v30, v48, 0x4b400000
	v_fmaak_f32 v42, v31, v48, 0x4b400000
	v_fmaak_f32 v43, v32, v48, 0x4b400000
	v_fmaak_f32 v44, v33, v48, 0x4b400000
	v_perm_b32 v41, v42, v41, s33
	v_perm_b32 v43, v44, v43, s34
	v_or_b32_e32 v46, v41, v43
	s_waitcnt vmcnt(0)
	ds_read_b128 v[18:21], v38 offset:0
	ds_read_b128 v[22:25], v38 offset:1024
	ds_read_b128 v[26:29], v38 offset:2048
	ds_read_b128 v[30:33], v38 offset:3072
	s_waitcnt lgkmcnt(0)
	s_barrier
	s_mov_b32 m0, s35
	s_nop 0
	global_load_lds_dwordx4 v34, s[16:17] nt
	global_load_lds_dwordx4 v34, s[16:17] offset:1024 nt
	global_load_lds_dwordx4 v34, s[16:17] offset:2048 nt
	global_load_lds_dwordx4 v35, s[16:17] offset:3072 nt
	s_add_u32 s16, s16, 0xfa0000
	s_addc_u32 s17, s17, 0
	v_cndmask_b32_e64 v30, 0, v30, s[18:19]
	v_cndmask_b32_e64 v31, 0, v31, s[18:19]
	v_cndmask_b32_e64 v32, 0, v32, s[18:19]
	v_cndmask_b32_e64 v33, 0, v33, s[18:19]
	v_max3_f32 v41, |v18|, |v19|, |v20|
	v_max3_f32 v42, |v21|, |v22|, |v23|
	v_max3_f32 v43, |v24|, |v25|, |v26|
	v_max3_f32 v44, |v27|, |v28|, |v29|
	v_max3_f32 v48, |v30|, |v31|, |v32|
	v_max3_f32 v41, v41, v42, |v33|
	v_max3_f32 v43, v43, v44, v48
	v_max_f32_e32 v41, v41, v43
	v_pk_add_f32 v[2:3], v[2:3], v[18:19]
	v_pk_add_f32 v[4:5], v[4:5], v[20:21]
	v_max_f32_dpp v41, v41, v41 quad_perm:[1,0,3,2] row_mask:0xf bank_mask:0xf
	v_pk_add_f32 v[6:7], v[6:7], v[22:23]
	v_pk_add_f32 v[8:9], v[8:9], v[24:25]
	v_max_f32_dpp v41, v41, v41 quad_perm:[2,3,0,1] row_mask:0xf bank_mask:0xf
	v_pk_add_f32 v[10:11], v[10:11], v[26:27]
	v_pk_add_f32 v[12:13], v[12:13], v[28:29]
	v_max_f32_dpp v41, v41, v41 row_half_mirror row_mask:0xf bank_mask:0xf
	v_pk_add_f32 v[14:15], v[14:15], v[30:31]
	v_pk_add_f32 v[16:17], v[16:17], v[32:33]
	v_max_f32_dpp v41, v41, v41 row_mirror row_mask:0xf bank_mask:0xf
	s_nop 1
	v_max_f32_dpp v41, v41, v41 row_bcast:15 row_mask:0xa bank_mask:0xf
	s_nop 1
	v_max_f32_dpp v41, v41, v41 row_bcast:31 row_mask:0xc bank_mask:0xf
	s_nop 1
	v_readlane_b32 s28, v41, 63
	s_nop 1
	v_div_scale_f32 v48, s[30:31], s28, s28, v47
	v_rcp_f32_e32 v49, v48
	s_nop 0
	v_fma_f32 v50, -v48, v49, 1.0
	v_fmac_f32_e32 v49, v50, v49
	v_mov_b32_e32 v50, s28
	v_div_scale_f32 v50, vcc, s32, v50, s32
	v_mul_f32_e32 v51, v50, v49
	v_fma_f32 v52, -v48, v51, v50
	v_fmac_f32_e32 v51, v52, v49
	v_fma_f32 v48, -v48, v51, v50
	v_div_fmas_f32 v48, v48, v49, v51
	v_div_fixup_f32 v48, v48, s28, v47
	v_cmp_gt_f32_e64 vcc, s28, 0
	v_writelane_b32 v40, s28, 19
	s_nop 0
	v_cndmask_b32_e32 v48, 0, v48, vcc
	v_fmaak_f32 v49, v18, v48, 0x4b400000
	v_fmaak_f32 v50, v19, v48, 0x4b400000
	v_fmaak_f32 v51, v20, v48, 0x4b400000
	v_fmaak_f32 v52, v21, v48, 0x4b400000
	v_perm_b32 v49, v50, v49, s33
	v_perm_b32 v51, v52, v51, s34
	v_or_b32_e32 v53, v49, v51
	v_fmaak_f32 v41, v22, v48, 0x4b400000
	v_fmaak_f32 v42, v23, v48, 0x4b400000
	v_fmaak_f32 v43, v24, v48, 0x4b400000
	v_fmaak_f32 v44, v25, v48, 0x4b400000
	v_perm_b32 v41, v42, v41, s33
	v_perm_b32 v43, v44, v43, s34
	v_or_b32_e32 v54, v41, v43
	v_fmaak_f32 v49, v26, v48, 0x4b400000
	v_fmaak_f32 v50, v27, v48, 0x4b400000
	v_fmaak_f32 v51, v28, v48, 0x4b400000
	v_fmaak_f32 v52, v29, v48, 0x4b400000
	v_perm_b32 v49, v50, v49, s33
	v_perm_b32 v51, v52, v51, s34
	v_or_b32_e32 v55, v49, v51
	v_fmaak_f32 v41, v30, v48, 0x4b400000
	v_fmaak_f32 v42, v31, v48, 0x4b400000
	v_fmaak_f32 v43, v32, v48, 0x4b400000
	v_fmaak_f32 v44, v33, v48, 0x4b400000
	v_perm_b32 v41, v42, v41, s33
	v_perm_b32 v43, v44, v43, s34
	v_or_b32_e32 v1, v41, v43
	s_waitcnt vmcnt(0)
	ds_read_b128 v[18:21], v38 offset:0
	ds_read_b128 v[22:25], v38 offset:1024
	ds_read_b128 v[26:29], v38 offset:2048
	ds_read_b128 v[30:33], v38 offset:3072
	s_waitcnt lgkmcnt(0)
	s_barrier
	s_mov_b32 m0, s35
	s_nop 0
	global_load_lds_dwordx4 v34, s[16:17] nt
	global_load_lds_dwordx4 v34, s[16:17] offset:1024 nt
	global_load_lds_dwordx4 v34, s[16:17] offset:2048 nt
	global_load_lds_dwordx4 v35, s[16:17] offset:3072 nt
	s_add_u32 s16, s16, 0xfa0000
	s_addc_u32 s17, s17, 0
	v_cndmask_b32_e64 v30, 0, v30, s[18:19]
	v_cndmask_b32_e64 v31, 0, v31, s[18:19]
	v_cndmask_b32_e64 v32, 0, v32, s[18:19]
	v_cndmask_b32_e64 v33, 0, v33, s[18:19]
	v_max3_f32 v41, |v18|, |v19|, |v20|
	v_max3_f32 v42, |v21|, |v22|, |v23|
	v_max3_f32 v43, |v24|, |v25|, |v26|
	v_max3_f32 v44, |v27|, |v28|, |v29|
	v_max3_f32 v48, |v30|, |v31|, |v32|
	v_max3_f32 v41, v41, v42, |v33|
	v_max3_f32 v43, v43, v44, v48
	v_max_f32_e32 v41, v41, v43
	v_pk_add_f32 v[2:3], v[2:3], v[18:19]
	v_pk_add_f32 v[4:5], v[4:5], v[20:21]
	v_max_f32_dpp v41, v41, v41 quad_perm:[1,0,3,2] row_mask:0xf bank_mask:0xf
	v_pk_add_f32 v[6:7], v[6:7], v[22:23]
	v_pk_add_f32 v[8:9], v[8:9], v[24:25]
	v_max_f32_dpp v41, v41, v41 quad_perm:[2,3,0,1] row_mask:0xf bank_mask:0xf
	v_pk_add_f32 v[10:11], v[10:11], v[26:27]
	v_pk_add_f32 v[12:13], v[12:13], v[28:29]
	v_max_f32_dpp v41, v41, v41 row_half_mirror row_mask:0xf bank_mask:0xf
	v_pk_add_f32 v[14:15], v[14:15], v[30:31]
	v_pk_add_f32 v[16:17], v[16:17], v[32:33]
	v_max_f32_dpp v41, v41, v41 row_mirror row_mask:0xf bank_mask:0xf
	s_nop 1
	v_max_f32_dpp v41, v41, v41 row_bcast:15 row_mask:0xa bank_mask:0xf
	s_nop 1
	v_max_f32_dpp v41, v41, v41 row_bcast:31 row_mask:0xc bank_mask:0xf
	s_nop 1
	v_readlane_b32 s28, v41, 63
	s_nop 1
	v_div_scale_f32 v48, s[30:31], s28, s28, v47
	v_rcp_f32_e32 v49, v48
	s_nop 0
	v_fma_f32 v50, -v48, v49, 1.0
	v_fmac_f32_e32 v49, v50, v49
	v_mov_b32_e32 v50, s28
	v_div_scale_f32 v50, vcc, s32, v50, s32
	v_mul_f32_e32 v51, v50, v49
	v_fma_f32 v52, -v48, v51, v50
	v_fmac_f32_e32 v51, v52, v49
	v_fma_f32 v48, -v48, v51, v50
	v_div_fmas_f32 v48, v48, v49, v51
	v_div_fixup_f32 v48, v48, s28, v47
	v_cmp_gt_f32_e64 vcc, s28, 0
	v_writelane_b32 v40, s28, 20
	s_nop 0
	v_cndmask_b32_e32 v48, 0, v48, vcc
	v_fmaak_f32 v49, v18, v48, 0x4b400000
	v_fmaak_f32 v50, v19, v48, 0x4b400000
	v_fmaak_f32 v51, v20, v48, 0x4b400000
	v_fmaak_f32 v52, v21, v48, 0x4b400000
	v_perm_b32 v49, v50, v49, s33
	v_perm_b32 v51, v52, v51, s34
	v_or_b32_e32 v49, v49, v51
	ds_write_b32 v38, v49 offset:4096
	v_fmaak_f32 v41, v22, v48, 0x4b400000
	v_fmaak_f32 v42, v23, v48, 0x4b400000
	v_fmaak_f32 v43, v24, v48, 0x4b400000
	v_fmaak_f32 v44, v25, v48, 0x4b400000
	v_perm_b32 v41, v42, v41, s33
	v_perm_b32 v43, v44, v43, s34
	v_or_b32_e32 v41, v41, v43
	ds_write_b32 v38, v41 offset:4100
	v_fmaak_f32 v49, v26, v48, 0x4b400000
	v_fmaak_f32 v50, v27, v48, 0x4b400000
	v_fmaak_f32 v51, v28, v48, 0x4b400000
	v_fmaak_f32 v52, v29, v48, 0x4b400000
	v_perm_b32 v49, v50, v49, s33
	v_perm_b32 v51, v52, v51, s34
	v_or_b32_e32 v49, v49, v51
	ds_write_b32 v38, v49 offset:4104
	v_fmaak_f32 v41, v30, v48, 0x4b400000
	v_fmaak_f32 v42, v31, v48, 0x4b400000
	v_fmaak_f32 v43, v32, v48, 0x4b400000
	v_fmaak_f32 v44, v33, v48, 0x4b400000
	v_perm_b32 v41, v42, v41, s33
	v_perm_b32 v43, v44, v43, s34
	v_or_b32_e32 v41, v41, v43
	ds_write_b32 v38, v41 offset:4108
	s_waitcnt vmcnt(0)
	ds_read_b128 v[18:21], v38 offset:0
	ds_read_b128 v[22:25], v38 offset:1024
	ds_read_b128 v[26:29], v38 offset:2048
	ds_read_b128 v[30:33], v38 offset:3072
	s_waitcnt lgkmcnt(0)
	s_barrier
	s_mov_b32 m0, s35
	s_nop 0
	global_load_lds_dwordx4 v34, s[16:17] nt
	global_load_lds_dwordx4 v34, s[16:17] offset:1024 nt
	global_load_lds_dwordx4 v34, s[16:17] offset:2048 nt
	global_load_lds_dwordx4 v35, s[16:17] offset:3072 nt
	s_add_u32 s16, s16, 0xfa0000
	s_addc_u32 s17, s17, 0
	v_cndmask_b32_e64 v30, 0, v30, s[18:19]
	v_cndmask_b32_e64 v31, 0, v31, s[18:19]
	v_cndmask_b32_e64 v32, 0, v32, s[18:19]
	v_cndmask_b32_e64 v33, 0, v33, s[18:19]
	v_max3_f32 v41, |v18|, |v19|, |v20|
	v_max3_f32 v42, |v21|, |v22|, |v23|
	v_max3_f32 v43, |v24|, |v25|, |v26|
	v_max3_f32 v44, |v27|, |v28|, |v29|
	v_max3_f32 v48, |v30|, |v31|, |v32|
	v_max3_f32 v41, v41, v42, |v33|
	v_max3_f32 v43, v43, v44, v48
	v_max_f32_e32 v41, v41, v43
	v_pk_add_f32 v[2:3], v[2:3], v[18:19]
	v_pk_add_f32 v[4:5], v[4:5], v[20:21]
	v_max_f32_dpp v41, v41, v41 quad_perm:[1,0,3,2] row_mask:0xf bank_mask:0xf
	v_pk_add_f32 v[6:7], v[6:7], v[22:23]
	v_pk_add_f32 v[8:9], v[8:9], v[24:25]
	v_max_f32_dpp v41, v41, v41 quad_perm:[2,3,0,1] row_mask:0xf bank_mask:0xf
	v_pk_add_f32 v[10:11], v[10:11], v[26:27]
	v_pk_add_f32 v[12:13], v[12:13], v[28:29]
	v_max_f32_dpp v41, v41, v41 row_half_mirror row_mask:0xf bank_mask:0xf
	v_pk_add_f32 v[14:15], v[14:15], v[30:31]
	v_pk_add_f32 v[16:17], v[16:17], v[32:33]
	v_max_f32_dpp v41, v41, v41 row_mirror row_mask:0xf bank_mask:0xf
	s_nop 1
	v_max_f32_dpp v41, v41, v41 row_bcast:15 row_mask:0xa bank_mask:0xf
	s_nop 1
	v_max_f32_dpp v41, v41, v41 row_bcast:31 row_mask:0xc bank_mask:0xf
	s_nop 1
	v_readlane_b32 s28, v41, 63
	s_nop 1
	v_div_scale_f32 v48, s[30:31], s28, s28, v47
	v_rcp_f32_e32 v49, v48
	s_nop 0
	v_fma_f32 v50, -v48, v49, 1.0
	v_fmac_f32_e32 v49, v50, v49
	v_mov_b32_e32 v50, s28
	v_div_scale_f32 v50, vcc, s32, v50, s32
	v_mul_f32_e32 v51, v50, v49
	v_fma_f32 v52, -v48, v51, v50
	v_fmac_f32_e32 v51, v52, v49
	v_fma_f32 v48, -v48, v51, v50
	v_div_fmas_f32 v48, v48, v49, v51
	v_div_fixup_f32 v48, v48, s28, v47
	v_cmp_gt_f32_e64 vcc, s28, 0
	v_writelane_b32 v40, s28, 21
	s_nop 0
	v_cndmask_b32_e32 v48, 0, v48, vcc
	v_fmaak_f32 v49, v18, v48, 0x4b400000
	v_fmaak_f32 v50, v19, v48, 0x4b400000
	v_fmaak_f32 v51, v20, v48, 0x4b400000
	v_fmaak_f32 v52, v21, v48, 0x4b400000
	v_perm_b32 v49, v50, v49, s33
	v_perm_b32 v51, v52, v51, s34
	v_or_b32_e32 v49, v49, v51
	ds_write_b32 v38, v49 offset:5120
	v_fmaak_f32 v41, v22, v48, 0x4b400000
	v_fmaak_f32 v42, v23, v48, 0x4b400000
	v_fmaak_f32 v43, v24, v48, 0x4b400000
	v_fmaak_f32 v44, v25, v48, 0x4b400000
	v_perm_b32 v41, v42, v41, s33
	v_perm_b32 v43, v44, v43, s34
	v_or_b32_e32 v41, v41, v43
	ds_write_b32 v38, v41 offset:5124
	v_fmaak_f32 v49, v26, v48, 0x4b400000
	v_fmaak_f32 v50, v27, v48, 0x4b400000
	v_fmaak_f32 v51, v28, v48, 0x4b400000
	v_fmaak_f32 v52, v29, v48, 0x4b400000
	v_perm_b32 v49, v50, v49, s33
	v_perm_b32 v51, v52, v51, s34
	v_or_b32_e32 v49, v49, v51
	ds_write_b32 v38, v49 offset:5128
	v_fmaak_f32 v41, v30, v48, 0x4b400000
	v_fmaak_f32 v42, v31, v48, 0x4b400000
	v_fmaak_f32 v43, v32, v48, 0x4b400000
	v_fmaak_f32 v44, v33, v48, 0x4b400000
	v_perm_b32 v41, v42, v41, s33
	v_perm_b32 v43, v44, v43, s34
	v_or_b32_e32 v41, v41, v43
	ds_write_b32 v38, v41 offset:5132
	s_waitcnt vmcnt(0)
	ds_read_b128 v[18:21], v38 offset:0
	ds_read_b128 v[22:25], v38 offset:1024
	ds_read_b128 v[26:29], v38 offset:2048
	ds_read_b128 v[30:33], v38 offset:3072
	s_waitcnt lgkmcnt(0)
	s_barrier
	s_mov_b32 m0, s35
	s_nop 0
	global_load_lds_dwordx4 v34, s[16:17] nt
	global_load_lds_dwordx4 v34, s[16:17] offset:1024 nt
	global_load_lds_dwordx4 v34, s[16:17] offset:2048 nt
	global_load_lds_dwordx4 v35, s[16:17] offset:3072 nt
	s_add_u32 s16, s16, 0xfa0000
	s_addc_u32 s17, s17, 0
	v_cndmask_b32_e64 v30, 0, v30, s[18:19]
	v_cndmask_b32_e64 v31, 0, v31, s[18:19]
	v_cndmask_b32_e64 v32, 0, v32, s[18:19]
	v_cndmask_b32_e64 v33, 0, v33, s[18:19]
	v_max3_f32 v41, |v18|, |v19|, |v20|
	v_max3_f32 v42, |v21|, |v22|, |v23|
	v_max3_f32 v43, |v24|, |v25|, |v26|
	v_max3_f32 v44, |v27|, |v28|, |v29|
	v_max3_f32 v48, |v30|, |v31|, |v32|
	v_max3_f32 v41, v41, v42, |v33|
	v_max3_f32 v43, v43, v44, v48
	v_max_f32_e32 v41, v41, v43
	v_pk_add_f32 v[2:3], v[2:3], v[18:19]
	v_pk_add_f32 v[4:5], v[4:5], v[20:21]
	v_max_f32_dpp v41, v41, v41 quad_perm:[1,0,3,2] row_mask:0xf bank_mask:0xf
	v_pk_add_f32 v[6:7], v[6:7], v[22:23]
	v_pk_add_f32 v[8:9], v[8:9], v[24:25]
	v_max_f32_dpp v41, v41, v41 quad_perm:[2,3,0,1] row_mask:0xf bank_mask:0xf
	v_pk_add_f32 v[10:11], v[10:11], v[26:27]
	v_pk_add_f32 v[12:13], v[12:13], v[28:29]
	v_max_f32_dpp v41, v41, v41 row_half_mirror row_mask:0xf bank_mask:0xf
	v_pk_add_f32 v[14:15], v[14:15], v[30:31]
	v_pk_add_f32 v[16:17], v[16:17], v[32:33]
	v_max_f32_dpp v41, v41, v41 row_mirror row_mask:0xf bank_mask:0xf
	s_nop 1
	v_max_f32_dpp v41, v41, v41 row_bcast:15 row_mask:0xa bank_mask:0xf
	s_nop 1
	v_max_f32_dpp v41, v41, v41 row_bcast:31 row_mask:0xc bank_mask:0xf
	s_nop 1
	v_readlane_b32 s28, v41, 63
	s_nop 1
	v_div_scale_f32 v48, s[30:31], s28, s28, v47
	v_rcp_f32_e32 v49, v48
	s_nop 0
	v_fma_f32 v50, -v48, v49, 1.0
	v_fmac_f32_e32 v49, v50, v49
	v_mov_b32_e32 v50, s28
	v_div_scale_f32 v50, vcc, s32, v50, s32
	v_mul_f32_e32 v51, v50, v49
	v_fma_f32 v52, -v48, v51, v50
	v_fmac_f32_e32 v51, v52, v49
	v_fma_f32 v48, -v48, v51, v50
	v_div_fmas_f32 v48, v48, v49, v51
	v_div_fixup_f32 v48, v48, s28, v47
	v_cmp_gt_f32_e64 vcc, s28, 0
	v_writelane_b32 v40, s28, 22
	s_nop 0
	v_cndmask_b32_e32 v48, 0, v48, vcc
	v_fmaak_f32 v49, v18, v48, 0x4b400000
	v_fmaak_f32 v50, v19, v48, 0x4b400000
	v_fmaak_f32 v51, v20, v48, 0x4b400000
	v_fmaak_f32 v52, v21, v48, 0x4b400000
	v_perm_b32 v49, v50, v49, s33
	v_perm_b32 v51, v52, v51, s34
	v_or_b32_e32 v49, v49, v51
	ds_write_b32 v38, v49 offset:6144
	v_fmaak_f32 v41, v22, v48, 0x4b400000
	v_fmaak_f32 v42, v23, v48, 0x4b400000
	v_fmaak_f32 v43, v24, v48, 0x4b400000
	v_fmaak_f32 v44, v25, v48, 0x4b400000
	v_perm_b32 v41, v42, v41, s33
	v_perm_b32 v43, v44, v43, s34
	v_or_b32_e32 v41, v41, v43
	ds_write_b32 v38, v41 offset:6148
	v_fmaak_f32 v49, v26, v48, 0x4b400000
	v_fmaak_f32 v50, v27, v48, 0x4b400000
	v_fmaak_f32 v51, v28, v48, 0x4b400000
	v_fmaak_f32 v52, v29, v48, 0x4b400000
	v_perm_b32 v49, v50, v49, s33
	v_perm_b32 v51, v52, v51, s34
	v_or_b32_e32 v49, v49, v51
	ds_write_b32 v38, v49 offset:6152
	v_fmaak_f32 v41, v30, v48, 0x4b400000
	v_fmaak_f32 v42, v31, v48, 0x4b400000
	v_fmaak_f32 v43, v32, v48, 0x4b400000
	v_fmaak_f32 v44, v33, v48, 0x4b400000
	v_perm_b32 v41, v42, v41, s33
	v_perm_b32 v43, v44, v43, s34
	v_or_b32_e32 v41, v41, v43
	ds_write_b32 v38, v41 offset:6156
	s_waitcnt vmcnt(0)
	ds_read_b128 v[18:21], v38 offset:0
	ds_read_b128 v[22:25], v38 offset:1024
	ds_read_b128 v[26:29], v38 offset:2048
	ds_read_b128 v[30:33], v38 offset:3072
	s_waitcnt lgkmcnt(0)
	s_cmp_eq_u32 s29, 1
	s_cbranch_scc0 .Lk1_nodma24
	s_mov_b32 m0, s35
	s_nop 0
	global_load_lds_dwordx4 v34, s[16:17] nt
	global_load_lds_dwordx4 v34, s[16:17] offset:1024 nt
	global_load_lds_dwordx4 v34, s[16:17] offset:2048 nt
	global_load_lds_dwordx4 v35, s[16:17] offset:3072 nt
	s_add_u32 s16, s16, 0xfa0000
	s_addc_u32 s17, s17, 0
.Lk1_nodma24:
	v_cndmask_b32_e64 v30, 0, v30, s[18:19]
	v_cndmask_b32_e64 v31, 0, v31, s[18:19]
	v_cndmask_b32_e64 v32, 0, v32, s[18:19]
	v_cndmask_b32_e64 v33, 0, v33, s[18:19]
	v_max3_f32 v41, |v18|, |v19|, |v20|
	v_max3_f32 v42, |v21|, |v22|, |v23|
	v_max3_f32 v43, |v24|, |v25|, |v26|
	v_max3_f32 v44, |v27|, |v28|, |v29|
	v_max3_f32 v48, |v30|, |v31|, |v32|
	v_max3_f32 v41, v41, v42, |v33|
	v_max3_f32 v43, v43, v44, v48
	v_max_f32_e32 v41, v41, v43
	v_pk_add_f32 v[2:3], v[2:3], v[18:19]
	v_pk_add_f32 v[4:5], v[4:5], v[20:21]
	v_max_f32_dpp v41, v41, v41 quad_perm:[1,0,3,2] row_mask:0xf bank_mask:0xf
	v_pk_add_f32 v[6:7], v[6:7], v[22:23]
	v_pk_add_f32 v[8:9], v[8:9], v[24:25]
	v_max_f32_dpp v41, v41, v41 quad_perm:[2,3,0,1] row_mask:0xf bank_mask:0xf
	v_pk_add_f32 v[10:11], v[10:11], v[26:27]
	v_pk_add_f32 v[12:13], v[12:13], v[28:29]
	v_max_f32_dpp v41, v41, v41 row_half_mirror row_mask:0xf bank_mask:0xf
	v_pk_add_f32 v[14:15], v[14:15], v[30:31]
	v_pk_add_f32 v[16:17], v[16:17], v[32:33]
	v_max_f32_dpp v41, v41, v41 row_mirror row_mask:0xf bank_mask:0xf
	s_nop 1
	v_max_f32_dpp v41, v41, v41 row_bcast:15 row_mask:0xa bank_mask:0xf
	s_nop 1
	v_max_f32_dpp v41, v41, v41 row_bcast:31 row_mask:0xc bank_mask:0xf
	s_nop 1
	v_readlane_b32 s28, v41, 63
	s_nop 1
	v_div_scale_f32 v48, s[30:31], s28, s28, v47
	v_rcp_f32_e32 v49, v48
	s_nop 0
	v_fma_f32 v50, -v48, v49, 1.0
	v_fmac_f32_e32 v49, v50, v49
	v_mov_b32_e32 v50, s28
	v_div_scale_f32 v50, vcc, s32, v50, s32
	v_mul_f32_e32 v51, v50, v49
	v_fma_f32 v52, -v48, v51, v50
	v_fmac_f32_e32 v51, v52, v49
	v_fma_f32 v48, -v48, v51, v50
	v_div_fmas_f32 v48, v48, v49, v51
	v_div_fixup_f32 v48, v48, s28, v47
	v_cmp_gt_f32_e64 vcc, s28, 0
	v_writelane_b32 v40, s28, 23
	s_nop 0
	v_cndmask_b32_e32 v48, 0, v48, vcc
	v_fmaak_f32 v49, v18, v48, 0x4b400000
	v_fmaak_f32 v50, v19, v48, 0x4b400000
	v_fmaak_f32 v51, v20, v48, 0x4b400000
	v_fmaak_f32 v52, v21, v48, 0x4b400000
	v_perm_b32 v49, v50, v49, s33
	v_perm_b32 v51, v52, v51, s34
	v_or_b32_e32 v49, v49, v51
	ds_write_b32 v38, v49 offset:7168
	v_fmaak_f32 v41, v22, v48, 0x4b400000
	v_fmaak_f32 v42, v23, v48, 0x4b400000
	v_fmaak_f32 v43, v24, v48, 0x4b400000
	v_fmaak_f32 v44, v25, v48, 0x4b400000
	v_perm_b32 v41, v42, v41, s33
	v_perm_b32 v43, v44, v43, s34
	v_or_b32_e32 v41, v41, v43
	ds_write_b32 v38, v41 offset:7172
	v_fmaak_f32 v49, v26, v48, 0x4b400000
	v_fmaak_f32 v50, v27, v48, 0x4b400000
	v_fmaak_f32 v51, v28, v48, 0x4b400000
	v_fmaak_f32 v52, v29, v48, 0x4b400000
	v_perm_b32 v49, v50, v49, s33
	v_perm_b32 v51, v52, v51, s34
	v_or_b32_e32 v49, v49, v51
	ds_write_b32 v38, v49 offset:7176
	v_fmaak_f32 v41, v30, v48, 0x4b400000
	v_fmaak_f32 v42, v31, v48, 0x4b400000
	v_fmaak_f32 v43, v32, v48, 0x4b400000
	v_fmaak_f32 v44, v33, v48, 0x4b400000
	v_perm_b32 v41, v42, v41, s33
	v_perm_b32 v43, v44, v43, s34
	v_or_b32_e32 v41, v41, v43
	ds_write_b32 v38, v41 offset:7180
	s_cmp_eq_u32 s29, 1
	s_cbranch_scc0 .Lk1_flush
	s_waitcnt vmcnt(0)
	ds_read_b128 v[18:21], v38 offset:0
	ds_read_b128 v[22:25], v38 offset:1024
	ds_read_b128 v[26:29], v38 offset:2048
	ds_read_b128 v[30:33], v38 offset:3072
	s_waitcnt lgkmcnt(0)
	v_cndmask_b32_e64 v30, 0, v30, s[18:19]
	v_cndmask_b32_e64 v31, 0, v31, s[18:19]
	v_cndmask_b32_e64 v32, 0, v32, s[18:19]
	v_cndmask_b32_e64 v33, 0, v33, s[18:19]
	v_max3_f32 v41, |v18|, |v19|, |v20|
	v_max3_f32 v42, |v21|, |v22|, |v23|
	v_max3_f32 v43, |v24|, |v25|, |v26|
	v_max3_f32 v44, |v27|, |v28|, |v29|
	v_max3_f32 v48, |v30|, |v31|, |v32|
	v_max3_f32 v41, v41, v42, |v33|
	v_max3_f32 v43, v43, v44, v48
	v_max_f32_e32 v41, v41, v43
	v_pk_add_f32 v[2:3], v[2:3], v[18:19]
	v_pk_add_f32 v[4:5], v[4:5], v[20:21]
	v_max_f32_dpp v41, v41, v41 quad_perm:[1,0,3,2] row_mask:0xf bank_mask:0xf
	v_pk_add_f32 v[6:7], v[6:7], v[22:23]
	v_pk_add_f32 v[8:9], v[8:9], v[24:25]
	v_max_f32_dpp v41, v41, v41 quad_perm:[2,3,0,1] row_mask:0xf bank_mask:0xf
	v_pk_add_f32 v[10:11], v[10:11], v[26:27]
	v_pk_add_f32 v[12:13], v[12:13], v[28:29]
	v_max_f32_dpp v41, v41, v41 row_half_mirror row_mask:0xf bank_mask:0xf
	v_pk_add_f32 v[14:15], v[14:15], v[30:31]
	v_pk_add_f32 v[16:17], v[16:17], v[32:33]
	v_max_f32_dpp v41, v41, v41 row_mirror row_mask:0xf bank_mask:0xf
	s_nop 1
	v_max_f32_dpp v41, v41, v41 row_bcast:15 row_mask:0xa bank_mask:0xf
	s_nop 1
	v_max_f32_dpp v41, v41, v41 row_bcast:31 row_mask:0xc bank_mask:0xf
	s_nop 1
	v_readlane_b32 s28, v41, 63
	s_nop 1
	v_div_scale_f32 v48, s[30:31], s28, s28, v47
	v_rcp_f32_e32 v49, v48
	s_nop 0
	v_fma_f32 v50, -v48, v49, 1.0
	v_fmac_f32_e32 v49, v50, v49
	v_mov_b32_e32 v50, s28
	v_div_scale_f32 v50, vcc, s32, v50, s32
	v_mul_f32_e32 v51, v50, v49
	v_fma_f32 v52, -v48, v51, v50
	v_fmac_f32_e32 v51, v52, v49
	v_fma_f32 v48, -v48, v51, v50
	v_div_fmas_f32 v48, v48, v49, v51
	v_div_fixup_f32 v48, v48, s28, v47
	v_cmp_gt_f32_e64 vcc, s28, 0
	v_writelane_b32 v40, s28, 24
	s_nop 0
	v_cndmask_b32_e32 v48, 0, v48, vcc
	v_fmaak_f32 v49, v18, v48, 0x4b400000
	v_fmaak_f32 v50, v19, v48, 0x4b400000
	v_fmaak_f32 v51, v20, v48, 0x4b400000
	v_fmaak_f32 v52, v21, v48, 0x4b400000
	v_perm_b32 v49, v50, v49, s33
	v_perm_b32 v51, v52, v51, s34
	v_or_b32_e32 v49, v49, v51
	s_add_u32 s20, s20, 0xc00000
	s_addc_u32 s21, s21, 0
	s_add_u32 s22, s22, 0xc00000
	s_addc_u32 s23, s23, 0
	s_add_u32 s24, s24, 0xc00000
	s_addc_u32 s25, s25, 0
	s_add_u32 s26, s26, 0xc00000
	s_addc_u32 s27, s27, 0
	global_store_dword v39, v49, s[20:21]
	v_fmaak_f32 v41, v22, v48, 0x4b400000
	v_fmaak_f32 v42, v23, v48, 0x4b400000
	v_fmaak_f32 v43, v24, v48, 0x4b400000
	v_fmaak_f32 v44, v25, v48, 0x4b400000
	v_perm_b32 v41, v42, v41, s33
	v_perm_b32 v43, v44, v43, s34
	v_or_b32_e32 v41, v41, v43
	global_store_dword v39, v41, s[22:23]
	v_fmaak_f32 v49, v26, v48, 0x4b400000
	v_fmaak_f32 v50, v27, v48, 0x4b400000
	v_fmaak_f32 v51, v28, v48, 0x4b400000
	v_fmaak_f32 v52, v29, v48, 0x4b400000
	v_perm_b32 v49, v50, v49, s33
	v_perm_b32 v51, v52, v51, s34
	v_or_b32_e32 v49, v49, v51
	global_store_dword v39, v49, s[24:25]
	v_fmaak_f32 v41, v30, v48, 0x4b400000
	v_fmaak_f32 v42, v31, v48, 0x4b400000
	v_fmaak_f32 v43, v32, v48, 0x4b400000
	v_fmaak_f32 v44, v33, v48, 0x4b400000
	v_perm_b32 v41, v42, v41, s33
	v_perm_b32 v43, v44, v43, s34
	v_or_b32_e32 v41, v41, v43
	global_store_dword v39, v41, s[26:27]
.Lk1_flush:
	s_barrier
	s_add_u32 s20, s40, 0x0
	s_addc_u32 s21, s41, 0
	s_add_u32 s22, s20, 0x186a000
	s_addc_u32 s23, s21, 0
	s_add_u32 s24, s22, 0x186a000
	s_addc_u32 s25, s23, 0
	s_add_u32 s26, s24, 0x186a000
	s_addc_u32 s27, s25, 0
	global_store_dword v39, v56, s[20:21] sc1
	global_store_dword v39, v57, s[22:23] sc1
	global_store_dword v39, v58, s[24:25] sc1
	global_store_dword v39, v59, s[26:27] sc1
	s_add_u32 s20, s20, 0x80000
	s_addc_u32 s21, s21, 0
	s_add_u32 s22, s22, 0x80000
	s_addc_u32 s23, s23, 0
	s_add_u32 s24, s24, 0x80000
	s_addc_u32 s25, s25, 0
	s_add_u32 s26, s26, 0x80000
	s_addc_u32 s27, s27, 0
	global_store_dword v39, v60, s[20:21] sc1
	global_store_dword v39, v61, s[22:23] sc1
	global_store_dword v39, v62, s[24:25] sc1
	global_store_dword v39, v63, s[26:27] sc1
	s_add_u32 s20, s20, 0x80000
	s_addc_u32 s21, s21, 0
	s_add_u32 s22, s22, 0x80000
	s_addc_u32 s23, s23, 0
	s_add_u32 s24, s24, 0x80000
	s_addc_u32 s25, s25, 0
	s_add_u32 s26, s26, 0x80000
	s_addc_u32 s27, s27, 0
	global_store_dword v39, v64, s[20:21] sc1
	global_store_dword v39, v65, s[22:23] sc1
	global_store_dword v39, v66, s[24:25] sc1
	global_store_dword v39, v67, s[26:27] sc1
	s_add_u32 s20, s20, 0x80000
	s_addc_u32 s21, s21, 0
	s_add_u32 s22, s22, 0x80000
	s_addc_u32 s23, s23, 0
	s_add_u32 s24, s24, 0x80000
	s_addc_u32 s25, s25, 0
	s_add_u32 s26, s26, 0x80000
	s_addc_u32 s27, s27, 0
	global_store_dword v39, v68, s[20:21] sc1
	global_store_dword v39, v69, s[22:23] sc1
	global_store_dword v39, v70, s[24:25] sc1
	global_store_dword v39, v71, s[26:27] sc1
	s_add_u32 s20, s20, 0x80000
	s_addc_u32 s21, s21, 0
	s_add_u32 s22, s22, 0x80000
	s_addc_u32 s23, s23, 0
	s_add_u32 s24, s24, 0x80000
	s_addc_u32 s25, s25, 0
	s_add_u32 s26, s26, 0x80000
	s_addc_u32 s27, s27, 0
	global_store_dword v39, v72, s[20:21] sc1
	global_store_dword v39, v73, s[22:23] sc1
	global_store_dword v39, v74, s[24:25] sc1
	global_store_dword v39, v75, s[26:27] sc1
	s_add_u32 s20, s20, 0x80000
	s_addc_u32 s21, s21, 0
	s_add_u32 s22, s22, 0x80000
	s_addc_u32 s23, s23, 0
	s_add_u32 s24, s24, 0x80000
	s_addc_u32 s25, s25, 0
	s_add_u32 s26, s26, 0x80000
	s_addc_u32 s27, s27, 0
	global_store_dword v39, v76, s[20:21] sc1
	global_store_dword v39, v77, s[22:23] sc1
	global_store_dword v39, v78, s[24:25] sc1
	global_store_dword v39, v79, s[26:27] sc1
	s_add_u32 s20, s20, 0x80000
	s_addc_u32 s21, s21, 0
	s_add_u32 s22, s22, 0x80000
	s_addc_u32 s23, s23, 0
	s_add_u32 s24, s24, 0x80000
	s_addc_u32 s25, s25, 0
	s_add_u32 s26, s26, 0x80000
	s_addc_u32 s27, s27, 0
	global_store_dword v39, v80, s[20:21] sc1
	global_store_dword v39, v81, s[22:23] sc1
	global_store_dword v39, v82, s[24:25] sc1
	global_store_dword v39, v83, s[26:27] sc1
	s_add_u32 s20, s20, 0x80000
	s_addc_u32 s21, s21, 0
	s_add_u32 s22, s22, 0x80000
	s_addc_u32 s23, s23, 0
	s_add_u32 s24, s24, 0x80000
	s_addc_u32 s25, s25, 0
	s_add_u32 s26, s26, 0x80000
	s_addc_u32 s27, s27, 0
	global_store_dword v39, v84, s[20:21] sc1
	global_store_dword v39, v85, s[22:23] sc1
	global_store_dword v39, v86, s[24:25] sc1
	global_store_dword v39, v87, s[26:27] sc1
	s_add_u32 s20, s20, 0x80000
	s_addc_u32 s21, s21, 0
	s_add_u32 s22, s22, 0x80000
	s_addc_u32 s23, s23, 0
	s_add_u32 s24, s24, 0x80000
	s_addc_u32 s25, s25, 0
	s_add_u32 s26, s26, 0x80000
	s_addc_u32 s27, s27, 0
	global_store_dword v39, v88, s[20:21] sc1
	global_store_dword v39, v89, s[22:23] sc1
	global_store_dword v39, v90, s[24:25] sc1
	global_store_dword v39, v91, s[26:27] sc1
	s_add_u32 s20, s20, 0x80000
	s_addc_u32 s21, s21, 0
	s_add_u32 s22, s22, 0x80000
	s_addc_u32 s23, s23, 0
	s_add_u32 s24, s24, 0x80000
	s_addc_u32 s25, s25, 0
	s_add_u32 s26, s26, 0x80000
	s_addc_u32 s27, s27, 0
	global_store_dword v39, v92, s[20:21] sc1
	global_store_dword v39, v93, s[22:23] sc1
	global_store_dword v39, v94, s[24:25] sc1
	global_store_dword v39, v95, s[26:27] sc1
	s_add_u32 s20, s20, 0x80000
	s_addc_u32 s21, s21, 0
	s_add_u32 s22, s22, 0x80000
	s_addc_u32 s23, s23, 0
	s_add_u32 s24, s24, 0x80000
	s_addc_u32 s25, s25, 0
	s_add_u32 s26, s26, 0x80000
	s_addc_u32 s27, s27, 0
	global_store_dword v39, v96, s[20:21] sc1
	global_store_dword v39, v97, s[22:23] sc1
	global_store_dword v39, v98, s[24:25] sc1
	global_store_dword v39, v99, s[26:27] sc1
	s_add_u32 s20, s20, 0x80000
	s_addc_u32 s21, s21, 0
	s_add_u32 s22, s22, 0x80000
	s_addc_u32 s23, s23, 0
	s_add_u32 s24, s24, 0x80000
	s_addc_u32 s25, s25, 0
	s_add_u32 s26, s26, 0x80000
	s_addc_u32 s27, s27, 0
	global_store_dword v39, v100, s[20:21] sc1
	global_store_dword v39, v101, s[22:23] sc1
	global_store_dword v39, v102, s[24:25] sc1
	global_store_dword v39, v103, s[26:27] sc1
	s_add_u32 s20, s20, 0x80000
	s_addc_u32 s21, s21, 0
	s_add_u32 s22, s22, 0x80000
	s_addc_u32 s23, s23, 0
	s_add_u32 s24, s24, 0x80000
	s_addc_u32 s25, s25, 0
	s_add_u32 s26, s26, 0x80000
	s_addc_u32 s27, s27, 0
	global_store_dword v39, v104, s[20:21] sc1
	global_store_dword v39, v105, s[22:23] sc1
	global_store_dword v39, v106, s[24:25] sc1
	global_store_dword v39, v107, s[26:27] sc1
	s_add_u32 s20, s20, 0x80000
	s_addc_u32 s21, s21, 0
	s_add_u32 s22, s22, 0x80000
	s_addc_u32 s23, s23, 0
	s_add_u32 s24, s24, 0x80000
	s_addc_u32 s25, s25, 0
	s_add_u32 s26, s26, 0x80000
	s_addc_u32 s27, s27, 0
	global_store_dword v39, v108, s[20:21] sc1
	global_store_dword v39, v109, s[22:23] sc1
	global_store_dword v39, v110, s[24:25] sc1
	global_store_dword v39, v111, s[26:27] sc1
	s_add_u32 s20, s20, 0x80000
	s_addc_u32 s21, s21, 0
	s_add_u32 s22, s22, 0x80000
	s_addc_u32 s23, s23, 0
	s_add_u32 s24, s24, 0x80000
	s_addc_u32 s25, s25, 0
	s_add_u32 s26, s26, 0x80000
	s_addc_u32 s27, s27, 0
	global_store_dword v39, v112, s[20:21] sc1
	global_store_dword v39, v113, s[22:23] sc1
	global_store_dword v39, v114, s[24:25] sc1
	global_store_dword v39, v115, s[26:27] sc1
	s_add_u32 s20, s20, 0x80000
	s_addc_u32 s21, s21, 0
	s_add_u32 s22, s22, 0x80000
	s_addc_u32 s23, s23, 0
	s_add_u32 s24, s24, 0x80000
	s_addc_u32 s25, s25, 0
	s_add_u32 s26, s26, 0x80000
	s_addc_u32 s27, s27, 0
	global_store_dword v39, v116, s[20:21] sc1
	global_store_dword v39, v117, s[22:23] sc1
	global_store_dword v39, v118, s[24:25] sc1
	global_store_dword v39, v119, s[26:27] sc1
	s_add_u32 s20, s20, 0x80000
	s_addc_u32 s21, s21, 0
	s_add_u32 s22, s22, 0x80000
	s_addc_u32 s23, s23, 0
	s_add_u32 s24, s24, 0x80000
	s_addc_u32 s25, s25, 0
	s_add_u32 s26, s26, 0x80000
	s_addc_u32 s27, s27, 0
	global_store_dword v39, v120, s[20:21] sc1
	global_store_dword v39, v121, s[22:23] sc1
	global_store_dword v39, v122, s[24:25] sc1
	global_store_dword v39, v123, s[26:27] sc1
	s_add_u32 s20, s20, 0x80000
	s_addc_u32 s21, s21, 0
	s_add_u32 s22, s22, 0x80000
	s_addc_u32 s23, s23, 0
	s_add_u32 s24, s24, 0x80000
	s_addc_u32 s25, s25, 0
	s_add_u32 s26, s26, 0x80000
	s_addc_u32 s27, s27, 0
	global_store_dword v39, v124, s[20:21] sc1
	global_store_dword v39, v125, s[22:23] sc1
	global_store_dword v39, v126, s[24:25] sc1
	global_store_dword v39, v127, s[26:27] sc1
	s_add_u32 s20, s20, 0x80000
	s_addc_u32 s21, s21, 0
	s_add_u32 s22, s22, 0x80000
	s_addc_u32 s23, s23, 0
	s_add_u32 s24, s24, 0x80000
	s_addc_u32 s25, s25, 0
	s_add_u32 s26, s26, 0x80000
	s_addc_u32 s27, s27, 0
	global_store_dword v39, v36, s[20:21] sc1
	global_store_dword v39, v37, s[22:23] sc1
	global_store_dword v39, v45, s[24:25] sc1
	global_store_dword v39, v46, s[26:27] sc1
	s_add_u32 s20, s20, 0x80000
	s_addc_u32 s21, s21, 0
	s_add_u32 s22, s22, 0x80000
	s_addc_u32 s23, s23, 0
	s_add_u32 s24, s24, 0x80000
	s_addc_u32 s25, s25, 0
	s_add_u32 s26, s26, 0x80000
	s_addc_u32 s27, s27, 0
	global_store_dword v39, v53, s[20:21] sc1
	global_store_dword v39, v54, s[22:23] sc1
	global_store_dword v39, v55, s[24:25] sc1
	global_store_dword v39, v1, s[26:27] sc1
	s_add_u32 s20, s20, 0x80000
	s_addc_u32 s21, s21, 0
	s_add_u32 s22, s22, 0x80000
	s_addc_u32 s23, s23, 0
	s_add_u32 s24, s24, 0x80000
	s_addc_u32 s25, s25, 0
	s_add_u32 s26, s26, 0x80000
	s_addc_u32 s27, s27, 0
	ds_read_b128 v[56:59], v38 offset:4096
	ds_read_b128 v[60:63], v38 offset:5120
	ds_read_b128 v[64:67], v38 offset:6144
	ds_read_b128 v[68:71], v38 offset:7168
	s_waitcnt lgkmcnt(0)
	global_store_dword v39, v56, s[20:21] sc1
	global_store_dword v39, v57, s[22:23] sc1
	global_store_dword v39, v58, s[24:25] sc1
	global_store_dword v39, v59, s[26:27] sc1
	s_add_u32 s20, s20, 0x80000
	s_addc_u32 s21, s21, 0
	s_add_u32 s22, s22, 0x80000
	s_addc_u32 s23, s23, 0
	s_add_u32 s24, s24, 0x80000
	s_addc_u32 s25, s25, 0
	s_add_u32 s26, s26, 0x80000
	s_addc_u32 s27, s27, 0
	global_store_dword v39, v60, s[20:21] sc1
	global_store_dword v39, v61, s[22:23] sc1
	global_store_dword v39, v62, s[24:25] sc1
	global_store_dword v39, v63, s[26:27] sc1
	s_add_u32 s20, s20, 0x80000
	s_addc_u32 s21, s21, 0
	s_add_u32 s22, s22, 0x80000
	s_addc_u32 s23, s23, 0
	s_add_u32 s24, s24, 0x80000
	s_addc_u32 s25, s25, 0
	s_add_u32 s26, s26, 0x80000
	s_addc_u32 s27, s27, 0
	global_store_dword v39, v64, s[20:21] sc1
	global_store_dword v39, v65, s[22:23] sc1
	global_store_dword v39, v66, s[24:25] sc1
	global_store_dword v39, v67, s[26:27] sc1
	s_add_u32 s20, s20, 0x80000
	s_addc_u32 s21, s21, 0
	s_add_u32 s22, s22, 0x80000
	s_addc_u32 s23, s23, 0
	s_add_u32 s24, s24, 0x80000
	s_addc_u32 s25, s25, 0
	s_add_u32 s26, s26, 0x80000
	s_addc_u32 s27, s27, 0
	global_store_dword v39, v68, s[20:21] sc1
	global_store_dword v39, v69, s[22:23] sc1
	global_store_dword v39, v70, s[24:25] sc1
	global_store_dword v39, v71, s[26:27] sc1
	v_mul_f32_e32 v40, 0x3c010204, v40
	v_and_b32_e32 v42, 63, v0
	v_lshlrev_b32_e32 v41, 14, v42
	s_mov_b32 s15, s12
	s_lshl_b32 s15, s15, 2
	s_add_u32 s8, s8, s15
	s_addc_u32 s9, s9, 0
	s_add_u32 s15, s29, 24
	v_cmp_gt_u32_e32 vcc, s15, v42
	s_and_saveexec_b64 s[38:39], vcc
	global_store_dword v41, v40, s[8:9]
	s_mov_b64 exec, s[38:39]
	s_lshl_b32 s15, s14, 12
	v_add_u32_e32 v41, s15, v34
	s_barrier
	ds_write_b128 v41, v[2:5]
	ds_write_b128 v41, v[6:9] offset:1024
	ds_write_b128 v41, v[10:13] offset:2048
	ds_write_b128 v41, v[14:17] offset:3072
	s_waitcnt lgkmcnt(0)
	s_barrier
	s_movk_i32 s15, 0x100
	v_cmp_gt_u32_e32 vcc, s15, v0
	s_and_saveexec_b64 s[38:39], vcc
	s_cbranch_execz .Lk1_end
	v_lshlrev_b32_e32 v16, 4, v0
	ds_read_b128 v[2:5], v16
	ds_read_b128 v[18:21], v16 offset:4096
	ds_read_b128 v[22:25], v16 offset:8192
	ds_read_b128 v[26:29], v16 offset:12288
	ds_read_b128 v[30:33], v16 offset:16384
	ds_read_b128 v[34:37], v16 offset:20480
	ds_read_b128 v[38:41], v16 offset:24576
	ds_read_b128 v[42:45], v16 offset:28672
	s_waitcnt lgkmcnt(6)
	v_pk_add_f32 v[2:3], v[2:3], v[18:19]
	v_pk_add_f32 v[4:5], v[4:5], v[20:21]
	s_waitcnt lgkmcnt(5)
	v_pk_add_f32 v[2:3], v[2:3], v[22:23]
	v_pk_add_f32 v[4:5], v[4:5], v[24:25]
	s_waitcnt lgkmcnt(4)
	v_pk_add_f32 v[2:3], v[2:3], v[26:27]
	v_pk_add_f32 v[4:5], v[4:5], v[28:29]
	s_waitcnt lgkmcnt(3)
	v_pk_add_f32 v[2:3], v[2:3], v[30:31]
	v_pk_add_f32 v[4:5], v[4:5], v[32:33]
	s_waitcnt lgkmcnt(2)
	v_pk_add_f32 v[2:3], v[2:3], v[34:35]
	v_pk_add_f32 v[4:5], v[4:5], v[36:37]
	s_waitcnt lgkmcnt(1)
	v_pk_add_f32 v[2:3], v[2:3], v[38:39]
	v_pk_add_f32 v[4:5], v[4:5], v[40:41]
	s_waitcnt lgkmcnt(0)
	v_pk_add_f32 v[2:3], v[2:3], v[42:43]
	v_pk_add_f32 v[4:5], v[4:5], v[44:45]
	s_lshl_b32 s15, s2, 12
	s_add_u32 s10, s10, s15
	s_addc_u32 s11, s11, 0
	global_store_dwordx4 v16, v[2:5], s[10:11]
